# speedup vs baseline: 1.0111x; 1.0111x over previous
.LBB3_35:
	s_andn2_b64 vcc, exec, s[2:3]
	s_cbranch_vccnz .LBB3_39
	s_waitcnt vmcnt(4)
	v_ashrrev_i32_e32 v81, 31, v80
	v_lshl_add_u64 v[2:3], v[80:81], 3, s[20:21]
	v_add_co_u32_e32 v2, vcc, 0x48000, v2
	s_movk_i32 s8, 0x620
	s_nop 0
	v_addc_co_u32_e32 v3, vcc, 0, v3, vcc
	global_load_dwordx2 v[82:83], v[2:3], off
	v_and_b32_e32 v2, 0x70, v7
	v_bitop3_b32 v2, v0, v2, 48 bitop3:0x6c
	s_waitcnt vmcnt(4)
	v_mad_u64_u32 v[64:65], s[6:7], v9, s8, v[2:3]
	v_lshrrev_b32_e32 v3, 4, v92
	v_bitop3_b32 v3, v3, v0, 4 bitop3:0x36
	v_lshlrev_b32_e32 v3, 4, v3
	v_and_b32_e32 v4, 0x70, v3
	s_waitcnt vmcnt(3)
	v_mad_u64_u32 v[66:67], s[6:7], v8, s8, v[4:5]
	s_waitcnt vmcnt(2)
	v_mad_u64_u32 v[68:69], s[6:7], v6, s8, v[2:3]
	s_waitcnt vmcnt(1)
	v_mad_u64_u32 v[70:71], s[6:7], v1, s8, v[4:5]
	v_lshrrev_b32_e32 v85, 5, v92
	v_bfe_u32 v2, v0, 1, 3
	s_mov_b64 s[6:7], 0x1800
	s_add_u32 s4, s20, 0x4000000
	v_bitop3_b32 v32, v85, v2, 2 bitop3:0x36
	v_bitop3_b32 v33, v85, v2, 4 bitop3:0x36
	v_bitop3_b32 v34, v85, v2, 6 bitop3:0x36
	v_lshl_add_u64 v[2:3], v[86:87], 0, s[6:7]
	s_addc_u32 s5, s21, 0
	s_lshl_b32 s2, s27, 12
	s_addk_i32 s2, 0x6000
	v_lshrrev_b32_e32 v1, 1, v0
	v_or_b32_e32 v81, s2, v84
	v_lshlrev_b32_e32 v0, 7, v0
	v_and_b32_e32 v8, 0xf80, v0
	v_lshlrev_b32_e32 v9, 4, v32
	v_bitop3_b32 v1, v85, v1, 7 bitop3:0x78
	v_or3_b32 v96, s2, v9, v8
	v_lshlrev_b32_e32 v9, 4, v33
	v_lshlrev_b32_e32 v1, 4, v1
	v_or3_b32 v97, s2, v9, v8
	v_lshlrev_b32_e32 v9, 4, v34
	v_or3_b32 v95, s2, v1, v8
	v_or3_b32 v94, s2, v9, v8
	v_add_u32_e32 v98, 0x103c0, v84
	global_load_dwordx4 v[116:119], v64, s[4:5] offset:0
	global_load_dwordx4 v[120:123], v66, s[4:5] offset:0
	global_load_dwordx4 v[124:127], v68, s[4:5] offset:0
	global_load_dwordx4 v[128:131], v70, s[4:5] offset:0
	global_load_dwordx4 v[132:135], v64, s[4:5] offset:128
	global_load_dwordx4 v[136:139], v66, s[4:5] offset:128
	global_load_dwordx4 v[140:143], v68, s[4:5] offset:128
	global_load_dwordx4 v[144:147], v70, s[4:5] offset:128
	global_load_dwordx4 v[148:151], v64, s[4:5] offset:256
	global_load_dwordx4 v[152:155], v66, s[4:5] offset:256
	global_load_dwordx4 v[156:159], v68, s[4:5] offset:256
	global_load_dwordx4 v[72:75], v70, s[4:5] offset:256
	s_add_u32 m0, s46, 0x0
	s_nop 0
	global_load_lds_dwordx4 v76, s[40:41]
	s_add_u32 m0, s47, 0x0
	s_nop 0
	global_load_lds_dwordx4 v77, s[42:43]
	s_add_u32 m0, s48, 0x0
	s_nop 0
	global_load_lds_dwordx4 v78, s[44:45]
	s_add_u32 m0, s46, 0x3000
	s_add_u32 s40, s40, 0x1800
	s_addc_u32 s41, s41, 0
	global_load_lds_dwordx4 v76, s[40:41]
	s_add_u32 m0, s47, 0x3000
	s_add_u32 s42, s42, 0x1800
	s_addc_u32 s43, s43, 0
	global_load_lds_dwordx4 v77, s[42:43]
	s_add_u32 m0, s48, 0x3000
	s_add_u32 s44, s44, 0x1800
	s_addc_u32 s45, s45, 0
	global_load_lds_dwordx4 v78, s[44:45]
	s_add_u32 m0, s46, 0xd3c0
	s_add_u32 s40, s40, 0x1800
	s_addc_u32 s41, s41, 0
	global_load_lds_dwordx4 v76, s[40:41]
	s_add_u32 m0, s47, 0xd3c0
	s_add_u32 s42, s42, 0x1800
	s_addc_u32 s43, s43, 0
	global_load_lds_dwordx4 v77, s[42:43]
	s_add_u32 m0, s48, 0xd3c0
	s_add_u32 s44, s44, 0x1800
	s_addc_u32 s45, s45, 0
	global_load_lds_dwordx4 v78, s[44:45]
	s_add_u32 m0, s46, 0x103c0
	s_add_u32 s40, s40, 0x1800
	s_addc_u32 s41, s41, 0
	global_load_lds_dwordx4 v76, s[40:41]
	s_add_u32 m0, s47, 0x103c0
	s_add_u32 s42, s42, 0x1800
	s_addc_u32 s43, s43, 0
	global_load_lds_dwordx4 v77, s[42:43]
	s_add_u32 m0, s48, 0x103c0
	s_add_u32 s44, s44, 0x1800
	s_addc_u32 s45, s45, 0
	global_load_lds_dwordx4 v78, s[44:45]
	s_waitcnt vmcnt(20)
	ds_write_b128 v81, v[116:119]
	ds_write_b128 v81, v[120:123] offset:1024
	ds_write_b128 v81, v[124:127] offset:2048
	ds_write_b128 v81, v[128:131] offset:3072
	ds_read_b128 v[52:55], v95
	ds_read_b128 v[56:59], v96
	ds_read_b128 v[60:63], v97
	ds_read_b128 v[0:3], v94
	global_load_dwordx4 v[116:119], v64, s[4:5] offset:384
	global_load_dwordx4 v[120:123], v66, s[4:5] offset:384
	global_load_dwordx4 v[124:127], v68, s[4:5] offset:384
	global_load_dwordx4 v[128:131], v70, s[4:5] offset:384
	s_waitcnt vmcnt(13)
	s_waitcnt lgkmcnt(0)
	s_barrier
	ds_read_b128 v[4:7], v84 offset:0
	ds_read_b128 v[8:11], v84 offset:1024
	ds_read_b128 v[12:15], v84 offset:2048
	ds_read_b128 v[16:19], v84 offset:3072
	ds_read_b128 v[20:23], v84 offset:4096
	ds_read_b128 v[24:27], v84 offset:5120
	ds_read_b128 v[28:31], v84 offset:6144
	ds_read_b128 v[32:35], v84 offset:7168
	ds_read_b128 v[36:39], v84 offset:8192
	ds_read_b128 v[40:43], v84 offset:9216
	ds_read_b128 v[44:47], v84 offset:10240
	ds_read_b128 v[48:51], v84 offset:11264
	s_waitcnt lgkmcnt(6)
	v_mfma_f32_32x32x16_f16 a[80:95], v[4:7], v[52:55], 0
	v_mfma_f32_32x32x16_f16 a[64:79], v[8:11], v[52:55], 0
	v_mfma_f32_32x32x16_f16 a[48:63], v[12:15], v[52:55], 0
	s_waitcnt vmcnt(10)
	s_waitcnt lgkmcnt(0)
	s_barrier
	s_nop 0
	v_mfma_f32_32x32x16_f16 a[32:47], v[16:19], v[52:55], 0
	ds_read_b128 v[4:7], v84 offset:12288
	ds_read_b128 v[8:11], v84 offset:13312
	v_mfma_f32_32x32x16_f16 a[16:31], v[20:23], v[52:55], 0
	ds_read_b128 v[12:15], v84 offset:14336
	ds_read_b128 v[16:19], v84 offset:15360
	v_mfma_f32_32x32x16_f16 a[0:15], v[24:27], v[52:55], 0
	ds_read_b128 v[20:23], v84 offset:16384
	ds_read_b128 v[24:27], v84 offset:17408
	v_mfma_f32_32x32x16_f16 a[80:95], v[28:31], v[56:59], a[80:95]
	s_add_u32 m0, s46, 0x0
	s_add_u32 s40, s40, 0x1800
	s_addc_u32 s41, s41, 0
	global_load_lds_dwordx4 v76, s[40:41]
	ds_read_b128 v[28:31], v84 offset:18432
	v_mfma_f32_32x32x16_f16 a[64:79], v[32:35], v[56:59], a[64:79]
	ds_read_b128 v[32:35], v84 offset:19456
	v_mfma_f32_32x32x16_f16 a[48:63], v[36:39], v[56:59], a[48:63]
	s_add_u32 m0, s47, 0x0
	s_add_u32 s42, s42, 0x1800
	s_addc_u32 s43, s43, 0
	global_load_lds_dwordx4 v77, s[42:43]
	ds_read_b128 v[36:39], v84 offset:20480
	v_mfma_f32_32x32x16_f16 a[32:47], v[40:43], v[56:59], a[32:47]
	ds_read_b128 v[40:43], v84 offset:21504
	v_mfma_f32_32x32x16_f16 a[16:31], v[44:47], v[56:59], a[16:31]
	s_add_u32 m0, s48, 0x0
	s_add_u32 s44, s44, 0x1800
	s_addc_u32 s45, s45, 0
	global_load_lds_dwordx4 v78, s[44:45]
	ds_read_b128 v[44:47], v84 offset:22528
	v_mfma_f32_32x32x16_f16 a[0:15], v[48:51], v[56:59], a[0:15]
	ds_read_b128 v[48:51], v84 offset:23552
	s_waitcnt lgkmcnt(6)
	s_nop 0
	v_mfma_f32_32x32x16_f16 a[80:95], v[4:7], v[60:63], a[80:95]
	s_waitcnt vmcnt(23)
	ds_write_b128 v81, v[132:135]
	ds_write_b128 v81, v[136:139] offset:1024
	ds_write_b128 v81, v[140:143] offset:2048
	ds_write_b128 v81, v[144:147] offset:3072
	s_nop 0
	v_mfma_f32_32x32x16_f16 a[64:79], v[8:11], v[60:63], a[64:79]
	ds_read_b128 v[100:103], v95
	ds_read_b128 v[104:107], v96
	ds_read_b128 v[108:111], v97
	ds_read_b128 v[112:115], v94
	v_mfma_f32_32x32x16_f16 a[48:63], v[12:15], v[60:63], a[48:63]
	global_load_dwordx4 v[132:135], v64, s[4:5] offset:512
	global_load_dwordx4 v[136:139], v66, s[4:5] offset:512
	global_load_dwordx4 v[140:143], v68, s[4:5] offset:512
	global_load_dwordx4 v[144:147], v70, s[4:5] offset:512
	s_waitcnt vmcnt(14)
	s_waitcnt lgkmcnt(8)
	s_barrier
	s_nop 0
	v_mfma_f32_32x32x16_f16 a[32:47], v[16:19], v[60:63], a[32:47]
	ds_read_b128 v[4:7], v84 offset:54208
	ds_read_b128 v[8:11], v84 offset:55232
	v_mfma_f32_32x32x16_f16 a[16:31], v[20:23], v[60:63], a[16:31]
	ds_read_b128 v[12:15], v84 offset:56256
	ds_read_b128 v[16:19], v84 offset:57280
	v_mfma_f32_32x32x16_f16 a[0:15], v[24:27], v[60:63], a[0:15]
	ds_read_b128 v[20:23], v84 offset:58304
	ds_read_b128 v[24:27], v84 offset:59328
	s_waitcnt lgkmcnt(6)
	s_nop 0
	v_mfma_f32_32x32x16_f16 a[80:95], v[28:31], v[0:3], a[80:95]
	s_add_u32 m0, s46, 0x3000
	s_add_u32 s40, s40, 0x1800
	s_addc_u32 s41, s41, 0
	global_load_lds_dwordx4 v76, s[40:41]
	ds_read_b128 v[28:31], v84 offset:60352
	s_nop 0
	v_mfma_f32_32x32x16_f16 a[64:79], v[32:35], v[0:3], a[64:79]
	ds_read_b128 v[32:35], v84 offset:61376
	v_mfma_f32_32x32x16_f16 a[48:63], v[36:39], v[0:3], a[48:63]
	s_add_u32 m0, s47, 0x3000
	s_add_u32 s42, s42, 0x1800
	s_addc_u32 s43, s43, 0
	global_load_lds_dwordx4 v77, s[42:43]
	ds_read_b128 v[36:39], v84 offset:62400
	s_nop 0
	v_mfma_f32_32x32x16_f16 a[32:47], v[40:43], v[0:3], a[32:47]
	ds_read_b128 v[40:43], v84 offset:63424
	v_mfma_f32_32x32x16_f16 a[16:31], v[44:47], v[0:3], a[16:31]
	s_add_u32 m0, s48, 0x3000
	s_add_u32 s44, s44, 0x1800
	s_addc_u32 s45, s45, 0
	global_load_lds_dwordx4 v78, s[44:45]
	ds_read_b128 v[44:47], v84 offset:64448
	s_nop 0
	v_mfma_f32_32x32x16_f16 a[0:15], v[48:51], v[0:3], a[0:15]
	ds_read_b128 v[48:51], v84 offset:65472
	s_waitcnt lgkmcnt(6)
	s_nop 0
	v_mfma_f32_32x32x16_f16 a[80:95], v[4:7], v[100:103], a[80:95]
	v_mfma_f32_32x32x16_f16 a[64:79], v[8:11], v[100:103], a[64:79]
	v_mfma_f32_32x32x16_f16 a[48:63], v[12:15], v[100:103], a[48:63]
	s_waitcnt vmcnt(14)
	s_waitcnt lgkmcnt(0)
	s_barrier
	s_nop 0
	v_mfma_f32_32x32x16_f16 a[32:47], v[16:19], v[100:103], a[32:47]
	ds_read_b128 v[4:7], v98
	ds_read_b128 v[8:11], v98 offset:1024
	v_mfma_f32_32x32x16_f16 a[16:31], v[20:23], v[100:103], a[16:31]
	ds_read_b128 v[12:15], v98 offset:2048
	ds_read_b128 v[16:19], v98 offset:3072
	v_mfma_f32_32x32x16_f16 a[0:15], v[24:27], v[100:103], a[0:15]
	ds_read_b128 v[20:23], v98 offset:4096
	ds_read_b128 v[24:27], v98 offset:5120
	v_mfma_f32_32x32x16_f16 a[80:95], v[28:31], v[104:107], a[80:95]
	s_add_u32 m0, s46, 0xd3c0
	s_add_u32 s40, s40, 0x1800
	s_addc_u32 s41, s41, 0
	global_load_lds_dwordx4 v76, s[40:41]
	ds_read_b128 v[28:31], v98 offset:6144
	s_nop 0
	v_mfma_f32_32x32x16_f16 a[64:79], v[32:35], v[104:107], a[64:79]
	ds_read_b128 v[32:35], v98 offset:7168
	v_mfma_f32_32x32x16_f16 a[48:63], v[36:39], v[104:107], a[48:63]
	s_add_u32 m0, s47, 0xd3c0
	s_add_u32 s42, s42, 0x1800
	s_addc_u32 s43, s43, 0
	global_load_lds_dwordx4 v77, s[42:43]
	ds_read_b128 v[36:39], v98 offset:8192
	s_nop 0
	v_mfma_f32_32x32x16_f16 a[32:47], v[40:43], v[104:107], a[32:47]
	ds_read_b128 v[40:43], v98 offset:9216
	v_mfma_f32_32x32x16_f16 a[16:31], v[44:47], v[104:107], a[16:31]
	s_add_u32 m0, s48, 0xd3c0
	s_add_u32 s44, s44, 0x1800
	s_addc_u32 s45, s45, 0
	global_load_lds_dwordx4 v78, s[44:45]
	ds_read_b128 v[44:47], v98 offset:10240
	s_nop 0
	v_mfma_f32_32x32x16_f16 a[0:15], v[48:51], v[104:107], a[0:15]
	ds_read_b128 v[48:51], v98 offset:11264
	s_waitcnt lgkmcnt(6)
	s_nop 0
	v_mfma_f32_32x32x16_f16 a[80:95], v[4:7], v[108:111], a[80:95]
	s_waitcnt vmcnt(29)
	ds_write_b128 v81, v[148:151]
	ds_write_b128 v81, v[152:155] offset:1024
	ds_write_b128 v81, v[156:159] offset:2048
	ds_write_b128 v81, v[72:75] offset:3072
	s_nop 0
	v_mfma_f32_32x32x16_f16 a[64:79], v[8:11], v[108:111], a[64:79]
	ds_read_b128 v[52:55], v95
	ds_read_b128 v[56:59], v96
	ds_read_b128 v[60:63], v97
	ds_read_b128 v[0:3], v94
	v_mfma_f32_32x32x16_f16 a[48:63], v[12:15], v[108:111], a[48:63]
	global_load_dwordx4 v[148:151], v64, s[4:5] offset:640
	global_load_dwordx4 v[152:155], v66, s[4:5] offset:640
	global_load_dwordx4 v[156:159], v68, s[4:5] offset:640
	global_load_dwordx4 v[72:75], v70, s[4:5] offset:640
	s_waitcnt vmcnt(14)
	s_waitcnt lgkmcnt(8)
	s_barrier
	s_nop 0
	v_mfma_f32_32x32x16_f16 a[32:47], v[16:19], v[108:111], a[32:47]
	ds_read_b128 v[4:7], v84 offset:0
	ds_read_b128 v[8:11], v84 offset:1024
	v_mfma_f32_32x32x16_f16 a[16:31], v[20:23], v[108:111], a[16:31]
	ds_read_b128 v[12:15], v84 offset:2048
	ds_read_b128 v[16:19], v84 offset:3072
	v_mfma_f32_32x32x16_f16 a[0:15], v[24:27], v[108:111], a[0:15]
	ds_read_b128 v[20:23], v84 offset:4096
	ds_read_b128 v[24:27], v84 offset:5120
	s_waitcnt lgkmcnt(6)
	s_nop 0
	v_mfma_f32_32x32x16_f16 a[80:95], v[28:31], v[112:115], a[80:95]
	s_add_u32 m0, s46, 0x103c0
	s_add_u32 s40, s40, 0x1800
	s_addc_u32 s41, s41, 0
	global_load_lds_dwordx4 v76, s[40:41]
	ds_read_b128 v[28:31], v84 offset:6144
	s_nop 0
	v_mfma_f32_32x32x16_f16 a[64:79], v[32:35], v[112:115], a[64:79]
	ds_read_b128 v[32:35], v84 offset:7168
	v_mfma_f32_32x32x16_f16 a[48:63], v[36:39], v[112:115], a[48:63]
	s_add_u32 m0, s47, 0x103c0
	s_add_u32 s42, s42, 0x1800
	s_addc_u32 s43, s43, 0
	global_load_lds_dwordx4 v77, s[42:43]
	ds_read_b128 v[36:39], v84 offset:8192
	s_nop 0
	v_mfma_f32_32x32x16_f16 a[32:47], v[40:43], v[112:115], a[32:47]
	ds_read_b128 v[40:43], v84 offset:9216
	v_mfma_f32_32x32x16_f16 a[16:31], v[44:47], v[112:115], a[16:31]
	s_add_u32 m0, s48, 0x103c0
	s_add_u32 s44, s44, 0x1800
	s_addc_u32 s45, s45, 0
	global_load_lds_dwordx4 v78, s[44:45]
	ds_read_b128 v[44:47], v84 offset:10240
	s_nop 0
	v_mfma_f32_32x32x16_f16 a[0:15], v[48:51], v[112:115], a[0:15]
	ds_read_b128 v[48:51], v84 offset:11264
	s_waitcnt lgkmcnt(6)
	s_nop 0
	v_mfma_f32_32x32x16_f16 a[80:95], v[4:7], v[52:55], a[80:95]
	v_mfma_f32_32x32x16_f16 a[64:79], v[8:11], v[52:55], a[64:79]
	v_mfma_f32_32x32x16_f16 a[48:63], v[12:15], v[52:55], a[48:63]
	s_waitcnt vmcnt(10)
	s_waitcnt lgkmcnt(0)
	s_barrier
	s_nop 0
	v_mfma_f32_32x32x16_f16 a[32:47], v[16:19], v[52:55], a[32:47]
	ds_read_b128 v[4:7], v84 offset:12288
	ds_read_b128 v[8:11], v84 offset:13312
	v_mfma_f32_32x32x16_f16 a[16:31], v[20:23], v[52:55], a[16:31]
	ds_read_b128 v[12:15], v84 offset:14336
	ds_read_b128 v[16:19], v84 offset:15360
	v_mfma_f32_32x32x16_f16 a[0:15], v[24:27], v[52:55], a[0:15]
	ds_read_b128 v[20:23], v84 offset:16384
	ds_read_b128 v[24:27], v84 offset:17408
	v_mfma_f32_32x32x16_f16 a[80:95], v[28:31], v[56:59], a[80:95]
	s_add_u32 m0, s46, 0x0
	s_add_u32 s40, s40, 0x1800
	s_addc_u32 s41, s41, 0
	global_load_lds_dwordx4 v76, s[40:41]
	ds_read_b128 v[28:31], v84 offset:18432
	v_mfma_f32_32x32x16_f16 a[64:79], v[32:35], v[56:59], a[64:79]
	ds_read_b128 v[32:35], v84 offset:19456
	v_mfma_f32_32x32x16_f16 a[48:63], v[36:39], v[56:59], a[48:63]
	s_add_u32 m0, s47, 0x0
	s_add_u32 s42, s42, 0x1800
	s_addc_u32 s43, s43, 0
	global_load_lds_dwordx4 v77, s[42:43]
	ds_read_b128 v[36:39], v84 offset:20480
	v_mfma_f32_32x32x16_f16 a[32:47], v[40:43], v[56:59], a[32:47]
	ds_read_b128 v[40:43], v84 offset:21504
	v_mfma_f32_32x32x16_f16 a[16:31], v[44:47], v[56:59], a[16:31]
	s_add_u32 m0, s48, 0x0
	s_add_u32 s44, s44, 0x1800
	s_addc_u32 s45, s45, 0
	global_load_lds_dwordx4 v78, s[44:45]
	ds_read_b128 v[44:47], v84 offset:22528
	v_mfma_f32_32x32x16_f16 a[0:15], v[48:51], v[56:59], a[0:15]
	ds_read_b128 v[48:51], v84 offset:23552
	s_waitcnt lgkmcnt(6)
	s_nop 0
	v_mfma_f32_32x32x16_f16 a[80:95], v[4:7], v[60:63], a[80:95]
	s_waitcnt vmcnt(23)
	ds_write_b128 v81, v[116:119]
	ds_write_b128 v81, v[120:123] offset:1024
	ds_write_b128 v81, v[124:127] offset:2048
	ds_write_b128 v81, v[128:131] offset:3072
	s_nop 0
	v_mfma_f32_32x32x16_f16 a[64:79], v[8:11], v[60:63], a[64:79]
	ds_read_b128 v[100:103], v95
	ds_read_b128 v[104:107], v96
	ds_read_b128 v[108:111], v97
	ds_read_b128 v[112:115], v94
	v_mfma_f32_32x32x16_f16 a[48:63], v[12:15], v[60:63], a[48:63]
	global_load_dwordx4 v[116:119], v64, s[4:5] offset:768
	global_load_dwordx4 v[120:123], v66, s[4:5] offset:768
	global_load_dwordx4 v[124:127], v68, s[4:5] offset:768
	global_load_dwordx4 v[128:131], v70, s[4:5] offset:768
	s_waitcnt vmcnt(14)
	s_waitcnt lgkmcnt(8)
	s_barrier
	s_nop 0
	v_mfma_f32_32x32x16_f16 a[32:47], v[16:19], v[60:63], a[32:47]
	ds_read_b128 v[4:7], v84 offset:54208
	ds_read_b128 v[8:11], v84 offset:55232
	v_mfma_f32_32x32x16_f16 a[16:31], v[20:23], v[60:63], a[16:31]
	ds_read_b128 v[12:15], v84 offset:56256
	ds_read_b128 v[16:19], v84 offset:57280
	v_mfma_f32_32x32x16_f16 a[0:15], v[24:27], v[60:63], a[0:15]
	ds_read_b128 v[20:23], v84 offset:58304
	ds_read_b128 v[24:27], v84 offset:59328
	s_waitcnt lgkmcnt(6)
	s_nop 0
	v_mfma_f32_32x32x16_f16 a[80:95], v[28:31], v[0:3], a[80:95]
	s_add_u32 m0, s46, 0x3000
	s_add_u32 s40, s40, 0x1800
	s_addc_u32 s41, s41, 0
	global_load_lds_dwordx4 v76, s[40:41]
	ds_read_b128 v[28:31], v84 offset:60352
	s_nop 0
	v_mfma_f32_32x32x16_f16 a[64:79], v[32:35], v[0:3], a[64:79]
	ds_read_b128 v[32:35], v84 offset:61376
	v_mfma_f32_32x32x16_f16 a[48:63], v[36:39], v[0:3], a[48:63]
	s_add_u32 m0, s47, 0x3000
	s_add_u32 s42, s42, 0x1800
	s_addc_u32 s43, s43, 0
	global_load_lds_dwordx4 v77, s[42:43]
	ds_read_b128 v[36:39], v84 offset:62400
	s_nop 0
	v_mfma_f32_32x32x16_f16 a[32:47], v[40:43], v[0:3], a[32:47]
	ds_read_b128 v[40:43], v84 offset:63424
	v_mfma_f32_32x32x16_f16 a[16:31], v[44:47], v[0:3], a[16:31]
	s_add_u32 m0, s48, 0x3000
	s_add_u32 s44, s44, 0x1800
	s_addc_u32 s45, s45, 0
	global_load_lds_dwordx4 v78, s[44:45]
	ds_read_b128 v[44:47], v84 offset:64448
	s_nop 0
	v_mfma_f32_32x32x16_f16 a[0:15], v[48:51], v[0:3], a[0:15]
	ds_read_b128 v[48:51], v84 offset:65472
	s_waitcnt lgkmcnt(6)
	s_nop 0
	v_mfma_f32_32x32x16_f16 a[80:95], v[4:7], v[100:103], a[80:95]
	v_mfma_f32_32x32x16_f16 a[64:79], v[8:11], v[100:103], a[64:79]
	v_mfma_f32_32x32x16_f16 a[48:63], v[12:15], v[100:103], a[48:63]
	s_waitcnt vmcnt(10)
	s_waitcnt lgkmcnt(0)
	s_barrier
	s_nop 0
	v_mfma_f32_32x32x16_f16 a[32:47], v[16:19], v[100:103], a[32:47]
	ds_read_b128 v[4:7], v98
	ds_read_b128 v[8:11], v98 offset:1024
	v_mfma_f32_32x32x16_f16 a[16:31], v[20:23], v[100:103], a[16:31]
	ds_read_b128 v[12:15], v98 offset:2048
	ds_read_b128 v[16:19], v98 offset:3072
	v_mfma_f32_32x32x16_f16 a[0:15], v[24:27], v[100:103], a[0:15]
	ds_read_b128 v[20:23], v98 offset:4096
	ds_read_b128 v[24:27], v98 offset:5120
	v_mfma_f32_32x32x16_f16 a[80:95], v[28:31], v[104:107], a[80:95]
	s_add_u32 m0, s46, 0xd3c0
	s_add_u32 s40, s40, 0x1800
	s_addc_u32 s41, s41, 0
	global_load_lds_dwordx4 v76, s[40:41]
	ds_read_b128 v[28:31], v98 offset:6144
	s_nop 0
	v_mfma_f32_32x32x16_f16 a[64:79], v[32:35], v[104:107], a[64:79]
	ds_read_b128 v[32:35], v98 offset:7168
	v_mfma_f32_32x32x16_f16 a[48:63], v[36:39], v[104:107], a[48:63]
	s_add_u32 m0, s47, 0xd3c0
	s_add_u32 s42, s42, 0x1800
	s_addc_u32 s43, s43, 0
	global_load_lds_dwordx4 v77, s[42:43]
	ds_read_b128 v[36:39], v98 offset:8192
	s_nop 0
	v_mfma_f32_32x32x16_f16 a[32:47], v[40:43], v[104:107], a[32:47]
	ds_read_b128 v[40:43], v98 offset:9216
	v_mfma_f32_32x32x16_f16 a[16:31], v[44:47], v[104:107], a[16:31]
	s_add_u32 m0, s48, 0xd3c0
	s_add_u32 s44, s44, 0x1800
	s_addc_u32 s45, s45, 0
	global_load_lds_dwordx4 v78, s[44:45]
	ds_read_b128 v[44:47], v98 offset:10240
	s_nop 0
	v_mfma_f32_32x32x16_f16 a[0:15], v[48:51], v[104:107], a[0:15]
	ds_read_b128 v[48:51], v98 offset:11264
	s_waitcnt lgkmcnt(6)
	s_nop 0
	v_mfma_f32_32x32x16_f16 a[80:95], v[4:7], v[108:111], a[80:95]
	s_waitcnt vmcnt(26)
	ds_write_b128 v81, v[132:135]
	ds_write_b128 v81, v[136:139] offset:1024
	ds_write_b128 v81, v[140:143] offset:2048
	ds_write_b128 v81, v[144:147] offset:3072
	s_nop 0
	v_mfma_f32_32x32x16_f16 a[64:79], v[8:11], v[108:111], a[64:79]
	ds_read_b128 v[52:55], v95
	ds_read_b128 v[56:59], v96
	ds_read_b128 v[60:63], v97
	ds_read_b128 v[0:3], v94
	v_mfma_f32_32x32x16_f16 a[48:63], v[12:15], v[108:111], a[48:63]
	global_load_dwordx4 v[132:135], v64, s[4:5] offset:896
	global_load_dwordx4 v[136:139], v66, s[4:5] offset:896
	global_load_dwordx4 v[140:143], v68, s[4:5] offset:896
	global_load_dwordx4 v[144:147], v70, s[4:5] offset:896
	s_waitcnt vmcnt(14)
	s_waitcnt lgkmcnt(8)
	s_barrier
	s_nop 0
	v_mfma_f32_32x32x16_f16 a[32:47], v[16:19], v[108:111], a[32:47]
	ds_read_b128 v[4:7], v84 offset:0
	ds_read_b128 v[8:11], v84 offset:1024
	v_mfma_f32_32x32x16_f16 a[16:31], v[20:23], v[108:111], a[16:31]
	ds_read_b128 v[12:15], v84 offset:2048
	ds_read_b128 v[16:19], v84 offset:3072
	v_mfma_f32_32x32x16_f16 a[0:15], v[24:27], v[108:111], a[0:15]
	ds_read_b128 v[20:23], v84 offset:4096
	ds_read_b128 v[24:27], v84 offset:5120
	s_waitcnt lgkmcnt(6)
	s_nop 0
	v_mfma_f32_32x32x16_f16 a[80:95], v[28:31], v[112:115], a[80:95]
	s_add_u32 m0, s46, 0x103c0
	s_add_u32 s40, s40, 0x1800
	s_addc_u32 s41, s41, 0
	global_load_lds_dwordx4 v76, s[40:41]
	ds_read_b128 v[28:31], v84 offset:6144
	s_nop 0
	v_mfma_f32_32x32x16_f16 a[64:79], v[32:35], v[112:115], a[64:79]
	ds_read_b128 v[32:35], v84 offset:7168
	v_mfma_f32_32x32x16_f16 a[48:63], v[36:39], v[112:115], a[48:63]
	s_add_u32 m0, s47, 0x103c0
	s_add_u32 s42, s42, 0x1800
	s_addc_u32 s43, s43, 0
	global_load_lds_dwordx4 v77, s[42:43]
	ds_read_b128 v[36:39], v84 offset:8192
	s_nop 0
	v_mfma_f32_32x32x16_f16 a[32:47], v[40:43], v[112:115], a[32:47]
	ds_read_b128 v[40:43], v84 offset:9216
	v_mfma_f32_32x32x16_f16 a[16:31], v[44:47], v[112:115], a[16:31]
	s_add_u32 m0, s48, 0x103c0
	s_add_u32 s44, s44, 0x1800
	s_addc_u32 s45, s45, 0
	global_load_lds_dwordx4 v78, s[44:45]
	ds_read_b128 v[44:47], v84 offset:10240
	s_nop 0
	v_mfma_f32_32x32x16_f16 a[0:15], v[48:51], v[112:115], a[0:15]
	ds_read_b128 v[48:51], v84 offset:11264
	s_waitcnt lgkmcnt(6)
	s_nop 0
	v_mfma_f32_32x32x16_f16 a[80:95], v[4:7], v[52:55], a[80:95]
	v_mfma_f32_32x32x16_f16 a[64:79], v[8:11], v[52:55], a[64:79]
	v_mfma_f32_32x32x16_f16 a[48:63], v[12:15], v[52:55], a[48:63]
	s_waitcnt vmcnt(10)
	s_waitcnt lgkmcnt(0)
	s_barrier
	s_nop 0
	v_mfma_f32_32x32x16_f16 a[32:47], v[16:19], v[52:55], a[32:47]
	ds_read_b128 v[4:7], v84 offset:12288
	ds_read_b128 v[8:11], v84 offset:13312
	v_mfma_f32_32x32x16_f16 a[16:31], v[20:23], v[52:55], a[16:31]
	ds_read_b128 v[12:15], v84 offset:14336
	ds_read_b128 v[16:19], v84 offset:15360
	v_mfma_f32_32x32x16_f16 a[0:15], v[24:27], v[52:55], a[0:15]
	ds_read_b128 v[20:23], v84 offset:16384
	ds_read_b128 v[24:27], v84 offset:17408
	v_mfma_f32_32x32x16_f16 a[80:95], v[28:31], v[56:59], a[80:95]
	s_add_u32 m0, s46, 0x0
	s_add_u32 s40, s40, 0x1800
	s_addc_u32 s41, s41, 0
	global_load_lds_dwordx4 v76, s[40:41]
	ds_read_b128 v[28:31], v84 offset:18432
	v_mfma_f32_32x32x16_f16 a[64:79], v[32:35], v[56:59], a[64:79]
	ds_read_b128 v[32:35], v84 offset:19456
	v_mfma_f32_32x32x16_f16 a[48:63], v[36:39], v[56:59], a[48:63]
	s_add_u32 m0, s47, 0x0
	s_add_u32 s42, s42, 0x1800
	s_addc_u32 s43, s43, 0
	global_load_lds_dwordx4 v77, s[42:43]
	ds_read_b128 v[36:39], v84 offset:20480
	v_mfma_f32_32x32x16_f16 a[32:47], v[40:43], v[56:59], a[32:47]
	ds_read_b128 v[40:43], v84 offset:21504
	v_mfma_f32_32x32x16_f16 a[16:31], v[44:47], v[56:59], a[16:31]
	s_add_u32 m0, s48, 0x0
	s_add_u32 s44, s44, 0x1800
	s_addc_u32 s45, s45, 0
	global_load_lds_dwordx4 v78, s[44:45]
	ds_read_b128 v[44:47], v84 offset:22528
	v_mfma_f32_32x32x16_f16 a[0:15], v[48:51], v[56:59], a[0:15]
	ds_read_b128 v[48:51], v84 offset:23552
	s_waitcnt lgkmcnt(6)
	s_nop 0
	v_mfma_f32_32x32x16_f16 a[80:95], v[4:7], v[60:63], a[80:95]
	s_waitcnt vmcnt(26)
	ds_write_b128 v81, v[148:151]
	ds_write_b128 v81, v[152:155] offset:1024
	ds_write_b128 v81, v[156:159] offset:2048
	ds_write_b128 v81, v[72:75] offset:3072
	s_nop 0
	v_mfma_f32_32x32x16_f16 a[64:79], v[8:11], v[60:63], a[64:79]
	ds_read_b128 v[100:103], v95
	ds_read_b128 v[104:107], v96
	ds_read_b128 v[108:111], v97
	ds_read_b128 v[112:115], v94
	v_mfma_f32_32x32x16_f16 a[48:63], v[12:15], v[60:63], a[48:63]
	global_load_dwordx4 v[148:151], v64, s[4:5] offset:1024
	global_load_dwordx4 v[152:155], v66, s[4:5] offset:1024
	global_load_dwordx4 v[156:159], v68, s[4:5] offset:1024
	global_load_dwordx4 v[72:75], v70, s[4:5] offset:1024
	s_waitcnt vmcnt(14)
	s_waitcnt lgkmcnt(8)
	s_barrier
	s_nop 0
	v_mfma_f32_32x32x16_f16 a[32:47], v[16:19], v[60:63], a[32:47]
	ds_read_b128 v[4:7], v84 offset:54208
	ds_read_b128 v[8:11], v84 offset:55232
	v_mfma_f32_32x32x16_f16 a[16:31], v[20:23], v[60:63], a[16:31]
	ds_read_b128 v[12:15], v84 offset:56256
	ds_read_b128 v[16:19], v84 offset:57280
	v_mfma_f32_32x32x16_f16 a[0:15], v[24:27], v[60:63], a[0:15]
	ds_read_b128 v[20:23], v84 offset:58304
	ds_read_b128 v[24:27], v84 offset:59328
	s_waitcnt lgkmcnt(6)
	s_nop 0
	v_mfma_f32_32x32x16_f16 a[80:95], v[28:31], v[0:3], a[80:95]
	s_add_u32 m0, s46, 0x3000
	s_add_u32 s40, s40, 0x1800
	s_addc_u32 s41, s41, 0
	global_load_lds_dwordx4 v76, s[40:41]
	ds_read_b128 v[28:31], v84 offset:60352
	s_nop 0
	v_mfma_f32_32x32x16_f16 a[64:79], v[32:35], v[0:3], a[64:79]
	ds_read_b128 v[32:35], v84 offset:61376
	v_mfma_f32_32x32x16_f16 a[48:63], v[36:39], v[0:3], a[48:63]
	s_add_u32 m0, s47, 0x3000
	s_add_u32 s42, s42, 0x1800
	s_addc_u32 s43, s43, 0
	global_load_lds_dwordx4 v77, s[42:43]
	ds_read_b128 v[36:39], v84 offset:62400
	s_nop 0
	v_mfma_f32_32x32x16_f16 a[32:47], v[40:43], v[0:3], a[32:47]
	ds_read_b128 v[40:43], v84 offset:63424
	v_mfma_f32_32x32x16_f16 a[16:31], v[44:47], v[0:3], a[16:31]
	s_add_u32 m0, s48, 0x3000
	s_add_u32 s44, s44, 0x1800
	s_addc_u32 s45, s45, 0
	global_load_lds_dwordx4 v78, s[44:45]
	ds_read_b128 v[44:47], v84 offset:64448
	s_nop 0
	v_mfma_f32_32x32x16_f16 a[0:15], v[48:51], v[0:3], a[0:15]
	ds_read_b128 v[48:51], v84 offset:65472
	s_waitcnt lgkmcnt(6)
	s_nop 0
	v_mfma_f32_32x32x16_f16 a[80:95], v[4:7], v[100:103], a[80:95]
	v_mfma_f32_32x32x16_f16 a[64:79], v[8:11], v[100:103], a[64:79]
	v_mfma_f32_32x32x16_f16 a[48:63], v[12:15], v[100:103], a[48:63]
	s_waitcnt vmcnt(10)
	s_waitcnt lgkmcnt(0)
	s_barrier
	s_nop 0
	v_mfma_f32_32x32x16_f16 a[32:47], v[16:19], v[100:103], a[32:47]
	ds_read_b128 v[4:7], v98
	ds_read_b128 v[8:11], v98 offset:1024
	v_mfma_f32_32x32x16_f16 a[16:31], v[20:23], v[100:103], a[16:31]
	ds_read_b128 v[12:15], v98 offset:2048
	ds_read_b128 v[16:19], v98 offset:3072
	v_mfma_f32_32x32x16_f16 a[0:15], v[24:27], v[100:103], a[0:15]
	ds_read_b128 v[20:23], v98 offset:4096
	ds_read_b128 v[24:27], v98 offset:5120
	v_mfma_f32_32x32x16_f16 a[80:95], v[28:31], v[104:107], a[80:95]
	s_add_u32 m0, s46, 0xd3c0
	s_add_u32 s40, s40, 0x1800
	s_addc_u32 s41, s41, 0
	global_load_lds_dwordx4 v76, s[40:41]
	ds_read_b128 v[28:31], v98 offset:6144
	s_nop 0
	v_mfma_f32_32x32x16_f16 a[64:79], v[32:35], v[104:107], a[64:79]
	ds_read_b128 v[32:35], v98 offset:7168
	v_mfma_f32_32x32x16_f16 a[48:63], v[36:39], v[104:107], a[48:63]
	s_add_u32 m0, s47, 0xd3c0
	s_add_u32 s42, s42, 0x1800
	s_addc_u32 s43, s43, 0
	global_load_lds_dwordx4 v77, s[42:43]
	ds_read_b128 v[36:39], v98 offset:8192
	s_nop 0
	v_mfma_f32_32x32x16_f16 a[32:47], v[40:43], v[104:107], a[32:47]
	ds_read_b128 v[40:43], v98 offset:9216
	v_mfma_f32_32x32x16_f16 a[16:31], v[44:47], v[104:107], a[16:31]
	s_add_u32 m0, s48, 0xd3c0
	s_add_u32 s44, s44, 0x1800
	s_addc_u32 s45, s45, 0
	global_load_lds_dwordx4 v78, s[44:45]
	ds_read_b128 v[44:47], v98 offset:10240
	s_nop 0
	v_mfma_f32_32x32x16_f16 a[0:15], v[48:51], v[104:107], a[0:15]
	ds_read_b128 v[48:51], v98 offset:11264
	s_waitcnt lgkmcnt(6)
	s_nop 0
	v_mfma_f32_32x32x16_f16 a[80:95], v[4:7], v[108:111], a[80:95]
	s_waitcnt vmcnt(26)
	ds_write_b128 v81, v[116:119]
	ds_write_b128 v81, v[120:123] offset:1024
	ds_write_b128 v81, v[124:127] offset:2048
	ds_write_b128 v81, v[128:131] offset:3072
	s_nop 0
	v_mfma_f32_32x32x16_f16 a[64:79], v[8:11], v[108:111], a[64:79]
	ds_read_b128 v[52:55], v95
	ds_read_b128 v[56:59], v96
	ds_read_b128 v[60:63], v97
	ds_read_b128 v[0:3], v94
	v_mfma_f32_32x32x16_f16 a[48:63], v[12:15], v[108:111], a[48:63]
	global_load_dwordx4 v[116:119], v64, s[4:5] offset:1152
	global_load_dwordx4 v[120:123], v66, s[4:5] offset:1152
	global_load_dwordx4 v[124:127], v68, s[4:5] offset:1152
	global_load_dwordx4 v[128:131], v70, s[4:5] offset:1152
	s_waitcnt vmcnt(14)
	s_waitcnt lgkmcnt(8)
	s_barrier
	s_nop 0
	v_mfma_f32_32x32x16_f16 a[32:47], v[16:19], v[108:111], a[32:47]
	ds_read_b128 v[4:7], v84 offset:0
	ds_read_b128 v[8:11], v84 offset:1024
	v_mfma_f32_32x32x16_f16 a[16:31], v[20:23], v[108:111], a[16:31]
	ds_read_b128 v[12:15], v84 offset:2048
	ds_read_b128 v[16:19], v84 offset:3072
	v_mfma_f32_32x32x16_f16 a[0:15], v[24:27], v[108:111], a[0:15]
	ds_read_b128 v[20:23], v84 offset:4096
	ds_read_b128 v[24:27], v84 offset:5120
	s_waitcnt lgkmcnt(6)
	s_nop 0
	v_mfma_f32_32x32x16_f16 a[80:95], v[28:31], v[112:115], a[80:95]
	s_add_u32 m0, s46, 0x103c0
	s_add_u32 s40, s40, 0x1800
	s_addc_u32 s41, s41, 0
	global_load_lds_dwordx4 v76, s[40:41]
	ds_read_b128 v[28:31], v84 offset:6144
	s_nop 0
	v_mfma_f32_32x32x16_f16 a[64:79], v[32:35], v[112:115], a[64:79]
	ds_read_b128 v[32:35], v84 offset:7168
	v_mfma_f32_32x32x16_f16 a[48:63], v[36:39], v[112:115], a[48:63]
	s_add_u32 m0, s47, 0x103c0
	s_add_u32 s42, s42, 0x1800
	s_addc_u32 s43, s43, 0
	global_load_lds_dwordx4 v77, s[42:43]
	ds_read_b128 v[36:39], v84 offset:8192
	s_nop 0
	v_mfma_f32_32x32x16_f16 a[32:47], v[40:43], v[112:115], a[32:47]
	ds_read_b128 v[40:43], v84 offset:9216
	v_mfma_f32_32x32x16_f16 a[16:31], v[44:47], v[112:115], a[16:31]
	s_add_u32 m0, s48, 0x103c0
	s_add_u32 s44, s44, 0x1800
	s_addc_u32 s45, s45, 0
	global_load_lds_dwordx4 v78, s[44:45]
	ds_read_b128 v[44:47], v84 offset:10240
	s_nop 0
	v_mfma_f32_32x32x16_f16 a[0:15], v[48:51], v[112:115], a[0:15]
	ds_read_b128 v[48:51], v84 offset:11264
	s_waitcnt lgkmcnt(6)
	s_nop 0
	v_mfma_f32_32x32x16_f16 a[80:95], v[4:7], v[52:55], a[80:95]
	v_mfma_f32_32x32x16_f16 a[64:79], v[8:11], v[52:55], a[64:79]
	v_mfma_f32_32x32x16_f16 a[48:63], v[12:15], v[52:55], a[48:63]
	s_waitcnt vmcnt(10)
	s_waitcnt lgkmcnt(0)
	s_barrier
	s_nop 0
	v_mfma_f32_32x32x16_f16 a[32:47], v[16:19], v[52:55], a[32:47]
	ds_read_b128 v[4:7], v84 offset:12288
	ds_read_b128 v[8:11], v84 offset:13312
	v_mfma_f32_32x32x16_f16 a[16:31], v[20:23], v[52:55], a[16:31]
	ds_read_b128 v[12:15], v84 offset:14336
	ds_read_b128 v[16:19], v84 offset:15360
	v_mfma_f32_32x32x16_f16 a[0:15], v[24:27], v[52:55], a[0:15]
	ds_read_b128 v[20:23], v84 offset:16384
	ds_read_b128 v[24:27], v84 offset:17408
	v_mfma_f32_32x32x16_f16 a[80:95], v[28:31], v[56:59], a[80:95]
	s_add_u32 m0, s46, 0x0
	s_add_u32 s40, s40, 0x1800
	s_addc_u32 s41, s41, 0
	global_load_lds_dwordx4 v76, s[40:41]
	ds_read_b128 v[28:31], v84 offset:18432
	v_mfma_f32_32x32x16_f16 a[64:79], v[32:35], v[56:59], a[64:79]
	ds_read_b128 v[32:35], v84 offset:19456
	v_mfma_f32_32x32x16_f16 a[48:63], v[36:39], v[56:59], a[48:63]
	s_add_u32 m0, s47, 0x0
	s_add_u32 s42, s42, 0x1800
	s_addc_u32 s43, s43, 0
	global_load_lds_dwordx4 v77, s[42:43]
	ds_read_b128 v[36:39], v84 offset:20480
	v_mfma_f32_32x32x16_f16 a[32:47], v[40:43], v[56:59], a[32:47]
	ds_read_b128 v[40:43], v84 offset:21504
	v_mfma_f32_32x32x16_f16 a[16:31], v[44:47], v[56:59], a[16:31]
	s_add_u32 m0, s48, 0x0
	s_add_u32 s44, s44, 0x1800
	s_addc_u32 s45, s45, 0
	global_load_lds_dwordx4 v78, s[44:45]
	ds_read_b128 v[44:47], v84 offset:22528
	v_mfma_f32_32x32x16_f16 a[0:15], v[48:51], v[56:59], a[0:15]
	ds_read_b128 v[48:51], v84 offset:23552
	s_waitcnt lgkmcnt(6)
	s_nop 0
	v_mfma_f32_32x32x16_f16 a[80:95], v[4:7], v[60:63], a[80:95]
	s_waitcnt vmcnt(26)
	ds_write_b128 v81, v[132:135]
	ds_write_b128 v81, v[136:139] offset:1024
	ds_write_b128 v81, v[140:143] offset:2048
	ds_write_b128 v81, v[144:147] offset:3072
	s_nop 0
	v_mfma_f32_32x32x16_f16 a[64:79], v[8:11], v[60:63], a[64:79]
	ds_read_b128 v[100:103], v95
	ds_read_b128 v[104:107], v96
	ds_read_b128 v[108:111], v97
	ds_read_b128 v[112:115], v94
	v_mfma_f32_32x32x16_f16 a[48:63], v[12:15], v[60:63], a[48:63]
	global_load_dwordx4 v[132:135], v64, s[4:5] offset:1280
	global_load_dwordx4 v[136:139], v66, s[4:5] offset:1280
	global_load_dwordx4 v[140:143], v68, s[4:5] offset:1280
	global_load_dwordx4 v[144:147], v70, s[4:5] offset:1280
	s_waitcnt vmcnt(14)
	s_waitcnt lgkmcnt(8)
	s_barrier
	s_nop 0
	v_mfma_f32_32x32x16_f16 a[32:47], v[16:19], v[60:63], a[32:47]
	ds_read_b128 v[4:7], v84 offset:54208
	ds_read_b128 v[8:11], v84 offset:55232
	v_mfma_f32_32x32x16_f16 a[16:31], v[20:23], v[60:63], a[16:31]
	ds_read_b128 v[12:15], v84 offset:56256
	ds_read_b128 v[16:19], v84 offset:57280
	v_mfma_f32_32x32x16_f16 a[0:15], v[24:27], v[60:63], a[0:15]
	ds_read_b128 v[20:23], v84 offset:58304
	ds_read_b128 v[24:27], v84 offset:59328
	s_waitcnt lgkmcnt(6)
	s_nop 0
	v_mfma_f32_32x32x16_f16 a[80:95], v[28:31], v[0:3], a[80:95]
	s_add_u32 m0, s46, 0x3000
	s_add_u32 s40, s40, 0x1800
	s_addc_u32 s41, s41, 0
	global_load_lds_dwordx4 v76, s[40:41]
	ds_read_b128 v[28:31], v84 offset:60352
	s_nop 0
	v_mfma_f32_32x32x16_f16 a[64:79], v[32:35], v[0:3], a[64:79]
	ds_read_b128 v[32:35], v84 offset:61376
	v_mfma_f32_32x32x16_f16 a[48:63], v[36:39], v[0:3], a[48:63]
	s_add_u32 m0, s47, 0x3000
	s_add_u32 s42, s42, 0x1800
	s_addc_u32 s43, s43, 0
	global_load_lds_dwordx4 v77, s[42:43]
	ds_read_b128 v[36:39], v84 offset:62400
	s_nop 0
	v_mfma_f32_32x32x16_f16 a[32:47], v[40:43], v[0:3], a[32:47]
	ds_read_b128 v[40:43], v84 offset:63424
	v_mfma_f32_32x32x16_f16 a[16:31], v[44:47], v[0:3], a[16:31]
	s_add_u32 m0, s48, 0x3000
	s_add_u32 s44, s44, 0x1800
	s_addc_u32 s45, s45, 0
	global_load_lds_dwordx4 v78, s[44:45]
	ds_read_b128 v[44:47], v84 offset:64448
	s_nop 0
	v_mfma_f32_32x32x16_f16 a[0:15], v[48:51], v[0:3], a[0:15]
	ds_read_b128 v[48:51], v84 offset:65472
	s_waitcnt lgkmcnt(6)
	s_nop 0
	v_mfma_f32_32x32x16_f16 a[80:95], v[4:7], v[100:103], a[80:95]
	v_mfma_f32_32x32x16_f16 a[64:79], v[8:11], v[100:103], a[64:79]
	v_mfma_f32_32x32x16_f16 a[48:63], v[12:15], v[100:103], a[48:63]
	s_waitcnt vmcnt(10)
	s_waitcnt lgkmcnt(0)
	s_barrier
	s_nop 0
	v_mfma_f32_32x32x16_f16 a[32:47], v[16:19], v[100:103], a[32:47]
	ds_read_b128 v[4:7], v98
	ds_read_b128 v[8:11], v98 offset:1024
	v_mfma_f32_32x32x16_f16 a[16:31], v[20:23], v[100:103], a[16:31]
	ds_read_b128 v[12:15], v98 offset:2048
	ds_read_b128 v[16:19], v98 offset:3072
	v_mfma_f32_32x32x16_f16 a[0:15], v[24:27], v[100:103], a[0:15]
	ds_read_b128 v[20:23], v98 offset:4096
	ds_read_b128 v[24:27], v98 offset:5120
	v_mfma_f32_32x32x16_f16 a[80:95], v[28:31], v[104:107], a[80:95]
	s_add_u32 m0, s46, 0xd3c0
	s_add_u32 s40, s40, 0x1800
	s_addc_u32 s41, s41, 0
	global_load_lds_dwordx4 v76, s[40:41]
	ds_read_b128 v[28:31], v98 offset:6144
	s_nop 0
	v_mfma_f32_32x32x16_f16 a[64:79], v[32:35], v[104:107], a[64:79]
	ds_read_b128 v[32:35], v98 offset:7168
	v_mfma_f32_32x32x16_f16 a[48:63], v[36:39], v[104:107], a[48:63]
	s_add_u32 m0, s47, 0xd3c0
	s_add_u32 s42, s42, 0x1800
	s_addc_u32 s43, s43, 0
	global_load_lds_dwordx4 v77, s[42:43]
	ds_read_b128 v[36:39], v98 offset:8192
	s_nop 0
	v_mfma_f32_32x32x16_f16 a[32:47], v[40:43], v[104:107], a[32:47]
	ds_read_b128 v[40:43], v98 offset:9216
	v_mfma_f32_32x32x16_f16 a[16:31], v[44:47], v[104:107], a[16:31]
	s_add_u32 m0, s48, 0xd3c0
	s_add_u32 s44, s44, 0x1800
	s_addc_u32 s45, s45, 0
	global_load_lds_dwordx4 v78, s[44:45]
	ds_read_b128 v[44:47], v98 offset:10240
	s_nop 0
	v_mfma_f32_32x32x16_f16 a[0:15], v[48:51], v[104:107], a[0:15]
	ds_read_b128 v[48:51], v98 offset:11264
	s_waitcnt lgkmcnt(6)
	s_nop 0
	v_mfma_f32_32x32x16_f16 a[80:95], v[4:7], v[108:111], a[80:95]
	s_waitcnt vmcnt(26)
	ds_write_b128 v81, v[148:151]
	ds_write_b128 v81, v[152:155] offset:1024
	ds_write_b128 v81, v[156:159] offset:2048
	ds_write_b128 v81, v[72:75] offset:3072
	s_nop 0
	v_mfma_f32_32x32x16_f16 a[64:79], v[8:11], v[108:111], a[64:79]
	ds_read_b128 v[52:55], v95
	ds_read_b128 v[56:59], v96
	ds_read_b128 v[60:63], v97
	ds_read_b128 v[0:3], v94
	v_mfma_f32_32x32x16_f16 a[48:63], v[12:15], v[108:111], a[48:63]
	global_load_dwordx4 v[148:151], v64, s[4:5] offset:1408
	global_load_dwordx4 v[152:155], v66, s[4:5] offset:1408
	global_load_dwordx4 v[156:159], v68, s[4:5] offset:1408
	global_load_dwordx4 v[72:75], v70, s[4:5] offset:1408
	s_waitcnt vmcnt(14)
	s_waitcnt lgkmcnt(8)
	s_barrier
	s_nop 0
	v_mfma_f32_32x32x16_f16 a[32:47], v[16:19], v[108:111], a[32:47]
	ds_read_b128 v[4:7], v84 offset:0
	ds_read_b128 v[8:11], v84 offset:1024
	v_mfma_f32_32x32x16_f16 a[16:31], v[20:23], v[108:111], a[16:31]
	ds_read_b128 v[12:15], v84 offset:2048
	ds_read_b128 v[16:19], v84 offset:3072
	v_mfma_f32_32x32x16_f16 a[0:15], v[24:27], v[108:111], a[0:15]
	ds_read_b128 v[20:23], v84 offset:4096
	ds_read_b128 v[24:27], v84 offset:5120
	s_waitcnt lgkmcnt(6)
	s_nop 0
	v_mfma_f32_32x32x16_f16 a[80:95], v[28:31], v[112:115], a[80:95]
	s_add_u32 m0, s46, 0x103c0
	s_add_u32 s40, s40, 0x1800
	s_addc_u32 s41, s41, 0
	global_load_lds_dwordx4 v76, s[40:41]
	ds_read_b128 v[28:31], v84 offset:6144
	s_nop 0
	v_mfma_f32_32x32x16_f16 a[64:79], v[32:35], v[112:115], a[64:79]
	ds_read_b128 v[32:35], v84 offset:7168
	v_mfma_f32_32x32x16_f16 a[48:63], v[36:39], v[112:115], a[48:63]
	s_add_u32 m0, s47, 0x103c0
	s_add_u32 s42, s42, 0x1800
	s_addc_u32 s43, s43, 0
	global_load_lds_dwordx4 v77, s[42:43]
	ds_read_b128 v[36:39], v84 offset:8192
	s_nop 0
	v_mfma_f32_32x32x16_f16 a[32:47], v[40:43], v[112:115], a[32:47]
	ds_read_b128 v[40:43], v84 offset:9216
	v_mfma_f32_32x32x16_f16 a[16:31], v[44:47], v[112:115], a[16:31]
	s_add_u32 m0, s48, 0x103c0
	s_add_u32 s44, s44, 0x1800
	s_addc_u32 s45, s45, 0
	global_load_lds_dwordx4 v78, s[44:45]
	ds_read_b128 v[44:47], v84 offset:10240
	s_nop 0
	v_mfma_f32_32x32x16_f16 a[0:15], v[48:51], v[112:115], a[0:15]
	ds_read_b128 v[48:51], v84 offset:11264
	s_waitcnt lgkmcnt(6)
	s_nop 0
	v_mfma_f32_32x32x16_f16 a[80:95], v[4:7], v[52:55], a[80:95]
	v_mfma_f32_32x32x16_f16 a[64:79], v[8:11], v[52:55], a[64:79]
	v_mfma_f32_32x32x16_f16 a[48:63], v[12:15], v[52:55], a[48:63]
	s_waitcnt vmcnt(10)
	s_waitcnt lgkmcnt(0)
	s_barrier
	s_nop 0
	v_mfma_f32_32x32x16_f16 a[32:47], v[16:19], v[52:55], a[32:47]
	ds_read_b128 v[4:7], v84 offset:12288
	ds_read_b128 v[8:11], v84 offset:13312
	v_mfma_f32_32x32x16_f16 a[16:31], v[20:23], v[52:55], a[16:31]
	ds_read_b128 v[12:15], v84 offset:14336
	ds_read_b128 v[16:19], v84 offset:15360
	v_mfma_f32_32x32x16_f16 a[0:15], v[24:27], v[52:55], a[0:15]
	ds_read_b128 v[20:23], v84 offset:16384
	ds_read_b128 v[24:27], v84 offset:17408
	v_mfma_f32_32x32x16_f16 a[80:95], v[28:31], v[56:59], a[80:95]
	s_add_u32 m0, s46, 0x0
	s_add_u32 s40, s40, 0x1800
	s_addc_u32 s41, s41, 0
	global_load_lds_dwordx4 v76, s[40:41]
	ds_read_b128 v[28:31], v84 offset:18432
	v_mfma_f32_32x32x16_f16 a[64:79], v[32:35], v[56:59], a[64:79]
	ds_read_b128 v[32:35], v84 offset:19456
	v_mfma_f32_32x32x16_f16 a[48:63], v[36:39], v[56:59], a[48:63]
	s_add_u32 m0, s47, 0x0
	s_add_u32 s42, s42, 0x1800
	s_addc_u32 s43, s43, 0
	global_load_lds_dwordx4 v77, s[42:43]
	ds_read_b128 v[36:39], v84 offset:20480
	v_mfma_f32_32x32x16_f16 a[32:47], v[40:43], v[56:59], a[32:47]
	ds_read_b128 v[40:43], v84 offset:21504
	v_mfma_f32_32x32x16_f16 a[16:31], v[44:47], v[56:59], a[16:31]
	s_add_u32 m0, s48, 0x0
	s_add_u32 s44, s44, 0x1800
	s_addc_u32 s45, s45, 0
	global_load_lds_dwordx4 v78, s[44:45]
	ds_read_b128 v[44:47], v84 offset:22528
	v_mfma_f32_32x32x16_f16 a[0:15], v[48:51], v[56:59], a[0:15]
	ds_read_b128 v[48:51], v84 offset:23552
	s_waitcnt lgkmcnt(6)
	s_nop 0
	v_mfma_f32_32x32x16_f16 a[80:95], v[4:7], v[60:63], a[80:95]
	s_waitcnt vmcnt(26)
	ds_write_b128 v81, v[116:119]
	ds_write_b128 v81, v[120:123] offset:1024
	ds_write_b128 v81, v[124:127] offset:2048
	ds_write_b128 v81, v[128:131] offset:3072
	s_nop 0
	v_mfma_f32_32x32x16_f16 a[64:79], v[8:11], v[60:63], a[64:79]
	ds_read_b128 v[100:103], v95
	ds_read_b128 v[104:107], v96
	ds_read_b128 v[108:111], v97
	ds_read_b128 v[112:115], v94
	v_mfma_f32_32x32x16_f16 a[48:63], v[12:15], v[60:63], a[48:63]
	global_load_dwordx4 v[116:119], v64, s[4:5] offset:1440
	global_load_dwordx4 v[120:123], v66, s[4:5] offset:1440
	global_load_dwordx4 v[124:127], v68, s[4:5] offset:1440
	global_load_dwordx4 v[128:131], v70, s[4:5] offset:1440
	s_waitcnt vmcnt(14)
	s_waitcnt lgkmcnt(8)
	s_barrier
	s_nop 0
	v_mfma_f32_32x32x16_f16 a[32:47], v[16:19], v[60:63], a[32:47]
	ds_read_b128 v[4:7], v84 offset:54208
	ds_read_b128 v[8:11], v84 offset:55232
	v_mfma_f32_32x32x16_f16 a[16:31], v[20:23], v[60:63], a[16:31]
	ds_read_b128 v[12:15], v84 offset:56256
	ds_read_b128 v[16:19], v84 offset:57280
	v_mfma_f32_32x32x16_f16 a[0:15], v[24:27], v[60:63], a[0:15]
	ds_read_b128 v[20:23], v84 offset:58304
	ds_read_b128 v[24:27], v84 offset:59328
	s_waitcnt lgkmcnt(6)
	s_nop 0
	v_mfma_f32_32x32x16_f16 a[80:95], v[28:31], v[0:3], a[80:95]
	s_add_u32 m0, s46, 0x3000
	s_add_u32 s40, s40, 0x1800
	s_addc_u32 s41, s41, 0
	global_load_lds_dwordx4 v76, s[40:41]
	ds_read_b128 v[28:31], v84 offset:60352
	s_nop 0
	v_mfma_f32_32x32x16_f16 a[64:79], v[32:35], v[0:3], a[64:79]
	ds_read_b128 v[32:35], v84 offset:61376
	v_mfma_f32_32x32x16_f16 a[48:63], v[36:39], v[0:3], a[48:63]
	s_add_u32 m0, s47, 0x3000
	s_add_u32 s42, s42, 0x1800
	s_addc_u32 s43, s43, 0
	global_load_lds_dwordx4 v77, s[42:43]
	ds_read_b128 v[36:39], v84 offset:62400
	s_nop 0
	v_mfma_f32_32x32x16_f16 a[32:47], v[40:43], v[0:3], a[32:47]
	ds_read_b128 v[40:43], v84 offset:63424
	v_mfma_f32_32x32x16_f16 a[16:31], v[44:47], v[0:3], a[16:31]
	s_add_u32 m0, s48, 0x3000
	s_add_u32 s44, s44, 0x1800
	s_addc_u32 s45, s45, 0
	global_load_lds_dwordx4 v78, s[44:45]
	ds_read_b128 v[44:47], v84 offset:64448
	s_nop 0
	v_mfma_f32_32x32x16_f16 a[0:15], v[48:51], v[0:3], a[0:15]
	ds_read_b128 v[48:51], v84 offset:65472
	s_waitcnt lgkmcnt(6)
	s_nop 0
	v_mfma_f32_32x32x16_f16 a[80:95], v[4:7], v[100:103], a[80:95]
	v_mfma_f32_32x32x16_f16 a[64:79], v[8:11], v[100:103], a[64:79]
	v_mfma_f32_32x32x16_f16 a[48:63], v[12:15], v[100:103], a[48:63]
	s_waitcnt vmcnt(10)
	s_waitcnt lgkmcnt(0)
	s_barrier
	s_nop 0
	v_mfma_f32_32x32x16_f16 a[32:47], v[16:19], v[100:103], a[32:47]
	ds_read_b128 v[4:7], v98
	ds_read_b128 v[8:11], v98 offset:1024
	v_mfma_f32_32x32x16_f16 a[16:31], v[20:23], v[100:103], a[16:31]
	ds_read_b128 v[12:15], v98 offset:2048
	ds_read_b128 v[16:19], v98 offset:3072
	v_mfma_f32_32x32x16_f16 a[0:15], v[24:27], v[100:103], a[0:15]
	ds_read_b128 v[20:23], v98 offset:4096
	ds_read_b128 v[24:27], v98 offset:5120
	v_mfma_f32_32x32x16_f16 a[80:95], v[28:31], v[104:107], a[80:95]
	s_add_u32 m0, s46, 0xd3c0
	s_add_u32 s40, s40, 0x1800
	s_addc_u32 s41, s41, 0
	global_load_lds_dwordx4 v76, s[40:41]
	ds_read_b128 v[28:31], v98 offset:6144
	s_nop 0
	v_mfma_f32_32x32x16_f16 a[64:79], v[32:35], v[104:107], a[64:79]
	ds_read_b128 v[32:35], v98 offset:7168
	v_mfma_f32_32x32x16_f16 a[48:63], v[36:39], v[104:107], a[48:63]
	s_add_u32 m0, s47, 0xd3c0
	s_add_u32 s42, s42, 0x1800
	s_addc_u32 s43, s43, 0
	global_load_lds_dwordx4 v77, s[42:43]
	ds_read_b128 v[36:39], v98 offset:8192
	s_nop 0
	v_mfma_f32_32x32x16_f16 a[32:47], v[40:43], v[104:107], a[32:47]
	ds_read_b128 v[40:43], v98 offset:9216
	v_mfma_f32_32x32x16_f16 a[16:31], v[44:47], v[104:107], a[16:31]
	s_add_u32 m0, s48, 0xd3c0
	s_add_u32 s44, s44, 0x1800
	s_addc_u32 s45, s45, 0
	global_load_lds_dwordx4 v78, s[44:45]
	ds_read_b128 v[44:47], v98 offset:10240
	s_nop 0
	v_mfma_f32_32x32x16_f16 a[0:15], v[48:51], v[104:107], a[0:15]
	ds_read_b128 v[48:51], v98 offset:11264
	s_waitcnt lgkmcnt(6)
	s_nop 0
	v_mfma_f32_32x32x16_f16 a[80:95], v[4:7], v[108:111], a[80:95]
	s_waitcnt vmcnt(26)
	ds_write_b128 v81, v[132:135]
	ds_write_b128 v81, v[136:139] offset:1024
	ds_write_b128 v81, v[140:143] offset:2048
	ds_write_b128 v81, v[144:147] offset:3072
	s_nop 0
	v_mfma_f32_32x32x16_f16 a[64:79], v[8:11], v[108:111], a[64:79]
	ds_read_b128 v[52:55], v95
	ds_read_b128 v[56:59], v96
	ds_read_b128 v[60:63], v97
	ds_read_b128 v[0:3], v94
	v_mfma_f32_32x32x16_f16 a[48:63], v[12:15], v[108:111], a[48:63]
	s_waitcnt vmcnt(10)
	s_waitcnt lgkmcnt(8)
	s_barrier
	s_nop 0
	v_mfma_f32_32x32x16_f16 a[32:47], v[16:19], v[108:111], a[32:47]
	ds_read_b128 v[4:7], v84 offset:0
	ds_read_b128 v[8:11], v84 offset:1024
	v_mfma_f32_32x32x16_f16 a[16:31], v[20:23], v[108:111], a[16:31]
	ds_read_b128 v[12:15], v84 offset:2048
	ds_read_b128 v[16:19], v84 offset:3072
	v_mfma_f32_32x32x16_f16 a[0:15], v[24:27], v[108:111], a[0:15]
	ds_read_b128 v[20:23], v84 offset:4096
	ds_read_b128 v[24:27], v84 offset:5120
	s_waitcnt lgkmcnt(6)
	s_nop 0
	v_mfma_f32_32x32x16_f16 a[80:95], v[28:31], v[112:115], a[80:95]
	s_add_u32 m0, s46, 0x103c0
	s_add_u32 s40, s40, 0x1800
	s_addc_u32 s41, s41, 0
	global_load_lds_dwordx4 v76, s[40:41]
	ds_read_b128 v[28:31], v84 offset:6144
	s_nop 0
	v_mfma_f32_32x32x16_f16 a[64:79], v[32:35], v[112:115], a[64:79]
	ds_read_b128 v[32:35], v84 offset:7168
	v_mfma_f32_32x32x16_f16 a[48:63], v[36:39], v[112:115], a[48:63]
	s_add_u32 m0, s47, 0x103c0
	s_add_u32 s42, s42, 0x1800
	s_addc_u32 s43, s43, 0
	global_load_lds_dwordx4 v77, s[42:43]
	ds_read_b128 v[36:39], v84 offset:8192
	s_nop 0
	v_mfma_f32_32x32x16_f16 a[32:47], v[40:43], v[112:115], a[32:47]
	ds_read_b128 v[40:43], v84 offset:9216
	v_mfma_f32_32x32x16_f16 a[16:31], v[44:47], v[112:115], a[16:31]
	s_add_u32 m0, s48, 0x103c0
	s_add_u32 s44, s44, 0x1800
	s_addc_u32 s45, s45, 0
	global_load_lds_dwordx4 v78, s[44:45]
	ds_read_b128 v[44:47], v84 offset:10240
	s_nop 0
	v_mfma_f32_32x32x16_f16 a[0:15], v[48:51], v[112:115], a[0:15]
	ds_read_b128 v[48:51], v84 offset:11264
	s_waitcnt lgkmcnt(6)
	s_nop 0
	v_mfma_f32_32x32x16_f16 a[80:95], v[4:7], v[52:55], a[80:95]
	v_mfma_f32_32x32x16_f16 a[64:79], v[8:11], v[52:55], a[64:79]
	v_mfma_f32_32x32x16_f16 a[48:63], v[12:15], v[52:55], a[48:63]
	s_waitcnt vmcnt(6)
	s_waitcnt lgkmcnt(0)
	s_barrier
	s_nop 0
	v_mfma_f32_32x32x16_f16 a[32:47], v[16:19], v[52:55], a[32:47]
	ds_read_b128 v[4:7], v84 offset:12288
	ds_read_b128 v[8:11], v84 offset:13312
	v_mfma_f32_32x32x16_f16 a[16:31], v[20:23], v[52:55], a[16:31]
	ds_read_b128 v[12:15], v84 offset:14336
	ds_read_b128 v[16:19], v84 offset:15360
	v_mfma_f32_32x32x16_f16 a[0:15], v[24:27], v[52:55], a[0:15]
	ds_read_b128 v[20:23], v84 offset:16384
	ds_read_b128 v[24:27], v84 offset:17408
	v_mfma_f32_32x32x16_f16 a[80:95], v[28:31], v[56:59], a[80:95]
	s_add_u32 m0, s46, 0x0
	s_add_u32 s40, s40, 0x1800
	s_addc_u32 s41, s41, 0
	global_load_lds_dwordx4 v76, s[40:41]
	ds_read_b128 v[28:31], v84 offset:18432
	v_mfma_f32_32x32x16_f16 a[64:79], v[32:35], v[56:59], a[64:79]
	ds_read_b128 v[32:35], v84 offset:19456
	v_mfma_f32_32x32x16_f16 a[48:63], v[36:39], v[56:59], a[48:63]
	s_add_u32 m0, s47, 0x0
	s_add_u32 s42, s42, s49
	s_addc_u32 s43, s43, 0
	global_load_lds_dwordx4 v77, s[42:43]
	ds_read_b128 v[36:39], v84 offset:20480
	s_nop 0
	v_mfma_f32_32x32x16_f16 a[32:47], v[40:43], v[56:59], a[32:47]
	ds_read_b128 v[40:43], v84 offset:21504
	v_mfma_f32_32x32x16_f16 a[16:31], v[44:47], v[56:59], a[16:31]
	s_add_u32 m0, s48, 0x0
	s_add_u32 s44, s44, 0xc00
	s_addc_u32 s45, s45, 0
	global_load_lds_dwordx4 v78, s[44:45]
	ds_read_b128 v[44:47], v84 offset:22528
	v_mfma_f32_32x32x16_f16 a[0:15], v[48:51], v[56:59], a[0:15]
	ds_read_b128 v[48:51], v84 offset:23552
	s_waitcnt lgkmcnt(6)
	s_nop 0
	v_mfma_f32_32x32x16_f16 a[80:95], v[4:7], v[60:63], a[80:95]
	s_waitcnt vmcnt(22)
	ds_write_b128 v81, v[148:151]
	ds_write_b128 v81, v[152:155] offset:1024
	ds_write_b128 v81, v[156:159] offset:2048
	ds_write_b128 v81, v[72:75] offset:3072
	s_nop 0
	v_mfma_f32_32x32x16_f16 a[64:79], v[8:11], v[60:63], a[64:79]
	ds_read_b128 v[100:103], v95
	ds_read_b128 v[104:107], v96
	ds_read_b128 v[108:111], v97
	ds_read_b128 v[112:115], v94
	v_mfma_f32_32x32x16_f16 a[48:63], v[12:15], v[60:63], a[48:63]
	s_waitcnt vmcnt(6)
	s_waitcnt lgkmcnt(8)
	s_barrier
	s_nop 0
	v_mfma_f32_32x32x16_f16 a[32:47], v[16:19], v[60:63], a[32:47]
	ds_read_b128 v[4:7], v84 offset:54208
	ds_read_b128 v[8:11], v84 offset:55232
	v_mfma_f32_32x32x16_f16 a[16:31], v[20:23], v[60:63], a[16:31]
	ds_read_b128 v[12:15], v84 offset:56256
	ds_read_b128 v[16:19], v84 offset:57280
	v_mfma_f32_32x32x16_f16 a[0:15], v[24:27], v[60:63], a[0:15]
	ds_read_b128 v[20:23], v84 offset:58304
	ds_read_b128 v[24:27], v84 offset:59328
	s_waitcnt lgkmcnt(6)
	s_nop 0
	v_mfma_f32_32x32x16_f16 a[80:95], v[28:31], v[0:3], a[80:95]
	ds_read_b128 v[28:31], v84 offset:60352
	v_mfma_f32_32x32x16_f16 a[64:79], v[32:35], v[0:3], a[64:79]
	ds_read_b128 v[32:35], v84 offset:61376
	v_mfma_f32_32x32x16_f16 a[48:63], v[36:39], v[0:3], a[48:63]
	ds_read_b128 v[36:39], v84 offset:62400
	v_mfma_f32_32x32x16_f16 a[32:47], v[40:43], v[0:3], a[32:47]
	ds_read_b128 v[40:43], v84 offset:63424
	v_mfma_f32_32x32x16_f16 a[16:31], v[44:47], v[0:3], a[16:31]
	ds_read_b128 v[44:47], v84 offset:64448
	v_mfma_f32_32x32x16_f16 a[0:15], v[48:51], v[0:3], a[0:15]
	ds_read_b128 v[48:51], v84 offset:65472
	s_waitcnt lgkmcnt(6)
	s_nop 0
	v_mfma_f32_32x32x16_f16 a[80:95], v[4:7], v[100:103], a[80:95]
	v_mfma_f32_32x32x16_f16 a[64:79], v[8:11], v[100:103], a[64:79]
	v_mfma_f32_32x32x16_f16 a[48:63], v[12:15], v[100:103], a[48:63]
	s_waitcnt vmcnt(3)
	s_waitcnt lgkmcnt(0)
	s_barrier
	s_nop 0
	v_mfma_f32_32x32x16_f16 a[32:47], v[16:19], v[100:103], a[32:47]
	ds_read_b128 v[4:7], v98
	ds_read_b128 v[8:11], v98 offset:1024
	v_mfma_f32_32x32x16_f16 a[16:31], v[20:23], v[100:103], a[16:31]
	ds_read_b128 v[12:15], v98 offset:2048
	ds_read_b128 v[16:19], v98 offset:3072
	v_mfma_f32_32x32x16_f16 a[0:15], v[24:27], v[100:103], a[0:15]
	ds_read_b128 v[20:23], v98 offset:4096
	ds_read_b128 v[24:27], v98 offset:5120
	v_mfma_f32_32x32x16_f16 a[80:95], v[28:31], v[104:107], a[80:95]
	ds_read_b128 v[28:31], v98 offset:6144
	v_mfma_f32_32x32x16_f16 a[64:79], v[32:35], v[104:107], a[64:79]
	ds_read_b128 v[32:35], v98 offset:7168
	v_mfma_f32_32x32x16_f16 a[48:63], v[36:39], v[104:107], a[48:63]
	ds_read_b128 v[36:39], v98 offset:8192
	v_mfma_f32_32x32x16_f16 a[32:47], v[40:43], v[104:107], a[32:47]
	ds_read_b128 v[40:43], v98 offset:9216
	v_mfma_f32_32x32x16_f16 a[16:31], v[44:47], v[104:107], a[16:31]
	ds_read_b128 v[44:47], v98 offset:10240
	v_mfma_f32_32x32x16_f16 a[0:15], v[48:51], v[104:107], a[0:15]
	ds_read_b128 v[48:51], v98 offset:11264
	s_waitcnt lgkmcnt(6)
	s_nop 0
	v_mfma_f32_32x32x16_f16 a[80:95], v[4:7], v[108:111], a[80:95]
	s_waitcnt vmcnt(12)
	ds_write_b128 v81, v[116:119]
	ds_write_b128 v81, v[120:123] offset:1024
	ds_write_b128 v81, v[124:127] offset:2048
	ds_write_b128 v81, v[128:131] offset:3072
	s_nop 0
	v_mfma_f32_32x32x16_f16 a[64:79], v[8:11], v[108:111], a[64:79]
	ds_read_b128 v[0:3], v94
	v_mfma_f32_32x32x16_f16 a[48:63], v[12:15], v[108:111], a[48:63]
	s_waitcnt vmcnt(0)
	s_waitcnt lgkmcnt(5)
	s_barrier
	s_nop 0
	v_mfma_f32_32x32x16_f16 a[32:47], v[16:19], v[108:111], a[32:47]
	ds_read_b128 v[4:7], v84 offset:0
	ds_read_b128 v[8:11], v84 offset:1024
	v_mfma_f32_32x32x16_f16 a[16:31], v[20:23], v[108:111], a[16:31]
	ds_read_b128 v[12:15], v84 offset:2048
	ds_read_b128 v[16:19], v84 offset:3072
	v_mfma_f32_32x32x16_f16 a[0:15], v[24:27], v[108:111], a[0:15]
	ds_read_b128 v[20:23], v84 offset:4096
	ds_read_b128 v[24:27], v84 offset:5120
	s_waitcnt lgkmcnt(6)
	s_nop 0
	v_mfma_f32_32x32x16_f16 a[80:95], v[28:31], v[112:115], a[80:95]
	v_mfma_f32_32x32x16_f16 a[64:79], v[32:35], v[112:115], a[64:79]
	v_mfma_f32_32x32x16_f16 a[48:63], v[36:39], v[112:115], a[48:63]
	v_mfma_f32_32x32x16_f16 a[32:47], v[40:43], v[112:115], a[32:47]
	v_mfma_f32_32x32x16_f16 a[16:31], v[44:47], v[112:115], a[16:31]
	v_mfma_f32_32x32x16_f16 a[0:15], v[48:51], v[112:115], a[0:15]
	s_waitcnt lgkmcnt(0)
	v_mfma_f32_32x32x16_f16 a[80:95], v[4:7], v[0:3], a[80:95]
	v_mfma_f32_32x32x16_f16 a[16:31], v[20:23], v[0:3], a[16:31]
	v_lshlrev_b32_e32 v22, 4, v85
	v_mfma_f32_32x32x16_f16 a[64:79], v[8:11], v[0:3], a[64:79]
	v_mfma_f32_32x32x16_f16 a[48:63], v[12:15], v[0:3], a[48:63]
	s_nop 7
	v_accvgpr_read_b32 v13, a88
	v_mfma_f32_32x32x16_f16 a[32:47], v[16:19], v[0:3], a[32:47]
	v_accvgpr_read_b32 v17, a92
	v_mfma_f32_32x32x16_f16 a[0:15], v[24:27], v[0:3], a[0:15]
	ds_read_b128 v[2:5], v22 offset:53248
	ds_read_b128 v[6:9], v22 offset:53280
	v_accvgpr_read_b32 v1, a80
	v_lshlrev_b32_e32 v0, 4, v92
	s_waitcnt lgkmcnt(1)
	v_add_f32_e32 v1, v1, v2
	v_accvgpr_read_b32 v2, a81
	v_add_f32_e32 v2, v3, v2
	v_max_f32_e32 v10, 0, v2
	v_accvgpr_read_b32 v2, a82
	v_add_f32_e32 v2, v4, v2
	v_max_f32_e32 v11, 0, v2
	v_accvgpr_read_b32 v2, a83
	v_add_f32_e32 v2, v5, v2
	v_max_f32_e32 v12, 0, v2
	v_accvgpr_read_b32 v2, a84
	s_waitcnt lgkmcnt(0)
	v_add_f32_e32 v2, v2, v6
	v_max_f32_e32 v6, 0, v2
	v_accvgpr_read_b32 v2, a85
	v_add_f32_e32 v2, v7, v2
	v_max_f32_e32 v7, 0, v2
	v_accvgpr_read_b32 v2, a86
	v_add_f32_e32 v2, v8, v2
	v_max_f32_e32 v8, 0, v2
	v_accvgpr_read_b32 v2, a87
	v_add_f32_e32 v2, v9, v2
	v_max_f32_e32 v9, 0, v2
	ds_read_b128 v[2:5], v22 offset:53312
	v_max_f32_e32 v1, 0, v1
	s_waitcnt lgkmcnt(0)
	v_add_f32_e32 v2, v13, v2
	v_max_f32_e32 v13, 0, v2
	v_accvgpr_read_b32 v2, a89
	v_add_f32_e32 v2, v3, v2
	v_max_f32_e32 v14, 0, v2
	v_accvgpr_read_b32 v2, a90
	v_add_f32_e32 v2, v4, v2
	v_max_f32_e32 v15, 0, v2
	v_accvgpr_read_b32 v2, a91
	v_add_f32_e32 v2, v5, v2
	v_max_f32_e32 v16, 0, v2
	ds_read_b128 v[2:5], v22 offset:53344
	s_waitcnt lgkmcnt(0)
	v_add_f32_e32 v2, v17, v2
	v_max_f32_e32 v17, 0, v2
	v_accvgpr_read_b32 v2, a93
	v_add_f32_e32 v2, v3, v2
	v_max_f32_e32 v18, 0, v2
	v_accvgpr_read_b32 v2, a94
	v_add_f32_e32 v2, v4, v2
	v_max_f32_e32 v19, 0, v2
	v_accvgpr_read_b32 v2, a95
	v_add_f32_e32 v2, v5, v2
	v_cvt_pk_f16_f32 v5, v8, v9
	v_cvt_pk_f16_f32 v4, v6, v7
	ds_read_b128 v[6:9], v0 offset:40960
	v_max_f32_e32 v20, 0, v2
	v_cvt_pk_f16_f32 v3, v11, v12
	v_cvt_pk_f16_f32 v2, v1, v10
	v_accvgpr_read_b32 v1, a64
	s_waitcnt lgkmcnt(0)
	v_mfma_f32_32x32x16_f16 a[80:95], v[6:9], v[2:5], 0
	ds_read_b128 v[6:9], v0 offset:41984
	v_cvt_pk_f16_f32 v5, v19, v20
	v_cvt_pk_f16_f32 v4, v17, v18
	v_cvt_pk_f16_f32 v3, v15, v16
	v_cvt_pk_f16_f32 v2, v13, v14
	v_accvgpr_read_b32 v13, a72
	v_accvgpr_read_b32 v17, a76
	s_waitcnt lgkmcnt(0)
	v_mfma_f32_32x32x16_f16 a[80:95], v[6:9], v[2:5], a[80:95]
	ds_read_b128 v[2:5], v22 offset:53376
	v_accvgpr_read_b32 v9, a68
	s_waitcnt lgkmcnt(0)
	v_add_f32_e32 v1, v1, v2
	v_accvgpr_read_b32 v2, a65
	v_add_f32_e32 v2, v3, v2
	v_max_f32_e32 v6, 0, v2
	v_accvgpr_read_b32 v2, a66
	v_add_f32_e32 v2, v4, v2
	v_max_f32_e32 v7, 0, v2
	v_accvgpr_read_b32 v2, a67
	v_add_f32_e32 v2, v5, v2
	v_max_f32_e32 v8, 0, v2
	ds_read_b128 v[2:5], v22 offset:53408
	v_max_f32_e32 v1, 0, v1
	s_waitcnt lgkmcnt(0)
	v_add_f32_e32 v2, v9, v2
	v_max_f32_e32 v9, 0, v2
	v_accvgpr_read_b32 v2, a69
	v_add_f32_e32 v2, v3, v2
	v_max_f32_e32 v10, 0, v2
	v_accvgpr_read_b32 v2, a70
	v_add_f32_e32 v2, v4, v2
	v_max_f32_e32 v11, 0, v2
	v_accvgpr_read_b32 v2, a71
	v_add_f32_e32 v2, v5, v2
	v_max_f32_e32 v12, 0, v2
	ds_read_b128 v[2:5], v22 offset:53440
	s_waitcnt lgkmcnt(0)
	v_add_f32_e32 v2, v13, v2
	v_max_f32_e32 v13, 0, v2
	v_accvgpr_read_b32 v2, a73
	v_add_f32_e32 v2, v3, v2
	v_max_f32_e32 v14, 0, v2
	v_accvgpr_read_b32 v2, a74
	v_add_f32_e32 v2, v4, v2
	v_max_f32_e32 v15, 0, v2
	v_accvgpr_read_b32 v2, a75
	v_add_f32_e32 v2, v5, v2
	v_max_f32_e32 v16, 0, v2
	ds_read_b128 v[2:5], v22 offset:53472
	s_waitcnt lgkmcnt(0)
	v_add_f32_e32 v2, v17, v2
	v_max_f32_e32 v17, 0, v2
	v_accvgpr_read_b32 v2, a77
	v_add_f32_e32 v2, v3, v2
	v_max_f32_e32 v18, 0, v2
	v_accvgpr_read_b32 v2, a78
	v_add_f32_e32 v2, v4, v2
	v_max_f32_e32 v19, 0, v2
	v_accvgpr_read_b32 v2, a79
	v_add_f32_e32 v2, v5, v2
	v_max_f32_e32 v20, 0, v2
	v_cvt_pk_f16_f32 v4, v9, v10
	v_cvt_pk_f16_f32 v3, v7, v8
	v_cvt_pk_f16_f32 v2, v1, v6
	ds_read_b128 v[6:9], v0 offset:43008
	v_cvt_pk_f16_f32 v5, v11, v12
	v_accvgpr_read_b32 v1, a48
	s_waitcnt lgkmcnt(0)
	v_mfma_f32_32x32x16_f16 a[80:95], v[6:9], v[2:5], a[80:95]
	ds_read_b128 v[6:9], v0 offset:44032
	v_cvt_pk_f16_f32 v5, v19, v20
	v_cvt_pk_f16_f32 v4, v17, v18
	v_cvt_pk_f16_f32 v3, v15, v16
	v_cvt_pk_f16_f32 v2, v13, v14
	v_accvgpr_read_b32 v13, a56
	v_accvgpr_read_b32 v17, a60
	s_waitcnt lgkmcnt(0)
	v_mfma_f32_32x32x16_f16 a[80:95], v[6:9], v[2:5], a[80:95]
	ds_read_b128 v[2:5], v22 offset:53504
	v_accvgpr_read_b32 v9, a52
	s_waitcnt lgkmcnt(0)
	v_add_f32_e32 v1, v1, v2
	v_accvgpr_read_b32 v2, a49
	v_add_f32_e32 v2, v3, v2
	v_max_f32_e32 v6, 0, v2
	v_accvgpr_read_b32 v2, a50
	v_add_f32_e32 v2, v4, v2
	v_max_f32_e32 v7, 0, v2
	v_accvgpr_read_b32 v2, a51
	v_add_f32_e32 v2, v5, v2
	v_max_f32_e32 v8, 0, v2
	ds_read_b128 v[2:5], v22 offset:53536
	v_max_f32_e32 v1, 0, v1
	s_waitcnt lgkmcnt(0)
	v_add_f32_e32 v2, v9, v2
	v_max_f32_e32 v9, 0, v2
	v_accvgpr_read_b32 v2, a53
	v_add_f32_e32 v2, v3, v2
	v_max_f32_e32 v10, 0, v2
	v_accvgpr_read_b32 v2, a54
	v_add_f32_e32 v2, v4, v2
	v_max_f32_e32 v11, 0, v2
	v_accvgpr_read_b32 v2, a55
	v_add_f32_e32 v2, v5, v2
	v_max_f32_e32 v12, 0, v2
	ds_read_b128 v[2:5], v22 offset:53568
	s_waitcnt lgkmcnt(0)
	v_add_f32_e32 v2, v13, v2
	v_max_f32_e32 v13, 0, v2
	v_accvgpr_read_b32 v2, a57
	v_add_f32_e32 v2, v3, v2
	v_max_f32_e32 v14, 0, v2
	v_accvgpr_read_b32 v2, a58
	v_add_f32_e32 v2, v4, v2
	v_max_f32_e32 v15, 0, v2
	v_accvgpr_read_b32 v2, a59
	v_add_f32_e32 v2, v5, v2
	v_max_f32_e32 v16, 0, v2
	ds_read_b128 v[2:5], v22 offset:53600
	s_waitcnt lgkmcnt(0)
	v_add_f32_e32 v2, v17, v2
	v_max_f32_e32 v17, 0, v2
	v_accvgpr_read_b32 v2, a61
	v_add_f32_e32 v2, v3, v2
	v_max_f32_e32 v18, 0, v2
	v_accvgpr_read_b32 v2, a62
	v_add_f32_e32 v2, v4, v2
	v_max_f32_e32 v19, 0, v2
	v_accvgpr_read_b32 v2, a63
	v_add_f32_e32 v2, v5, v2
	v_max_f32_e32 v20, 0, v2
	v_cvt_pk_f16_f32 v4, v9, v10
	v_cvt_pk_f16_f32 v3, v7, v8
	v_cvt_pk_f16_f32 v2, v1, v6
	ds_read_b128 v[6:9], v0 offset:45056
	v_cvt_pk_f16_f32 v5, v11, v12
	v_accvgpr_read_b32 v1, a32
	s_waitcnt lgkmcnt(0)
	v_mfma_f32_32x32x16_f16 a[80:95], v[6:9], v[2:5], a[80:95]
	ds_read_b128 v[6:9], v0 offset:46080
	v_cvt_pk_f16_f32 v5, v19, v20
	v_cvt_pk_f16_f32 v4, v17, v18
	v_cvt_pk_f16_f32 v3, v15, v16
	v_cvt_pk_f16_f32 v2, v13, v14
	v_accvgpr_read_b32 v13, a40
	v_accvgpr_read_b32 v17, a44
	s_waitcnt lgkmcnt(0)
	v_mfma_f32_32x32x16_f16 a[80:95], v[6:9], v[2:5], a[80:95]
	ds_read_b128 v[2:5], v22 offset:53632
	v_accvgpr_read_b32 v9, a36
	s_waitcnt lgkmcnt(0)
	v_add_f32_e32 v1, v1, v2
	v_accvgpr_read_b32 v2, a33
	v_add_f32_e32 v2, v3, v2
	v_max_f32_e32 v6, 0, v2
	v_accvgpr_read_b32 v2, a34
	v_add_f32_e32 v2, v4, v2
	v_max_f32_e32 v7, 0, v2
	v_accvgpr_read_b32 v2, a35
	v_add_f32_e32 v2, v5, v2
	v_max_f32_e32 v8, 0, v2
	ds_read_b128 v[2:5], v22 offset:53664
	v_max_f32_e32 v1, 0, v1
	s_waitcnt lgkmcnt(0)
	v_add_f32_e32 v2, v9, v2
	v_max_f32_e32 v9, 0, v2
	v_accvgpr_read_b32 v2, a37
	v_add_f32_e32 v2, v3, v2
	v_max_f32_e32 v10, 0, v2
	v_accvgpr_read_b32 v2, a38
	v_add_f32_e32 v2, v4, v2
	v_max_f32_e32 v11, 0, v2
	v_accvgpr_read_b32 v2, a39
	v_add_f32_e32 v2, v5, v2
	v_max_f32_e32 v12, 0, v2
	ds_read_b128 v[2:5], v22 offset:53696
	s_waitcnt lgkmcnt(0)
	v_add_f32_e32 v2, v13, v2
	v_max_f32_e32 v13, 0, v2
	v_accvgpr_read_b32 v2, a41
	v_add_f32_e32 v2, v3, v2
	v_max_f32_e32 v14, 0, v2
	v_accvgpr_read_b32 v2, a42
	v_add_f32_e32 v2, v4, v2
	v_max_f32_e32 v15, 0, v2
	v_accvgpr_read_b32 v2, a43
	v_add_f32_e32 v2, v5, v2
	v_max_f32_e32 v16, 0, v2
	ds_read_b128 v[2:5], v22 offset:53728
	s_waitcnt lgkmcnt(0)
	v_add_f32_e32 v2, v17, v2
	v_max_f32_e32 v17, 0, v2
	v_accvgpr_read_b32 v2, a45
	v_add_f32_e32 v2, v3, v2
	v_max_f32_e32 v18, 0, v2
	v_accvgpr_read_b32 v2, a46
	v_add_f32_e32 v2, v4, v2
	v_max_f32_e32 v19, 0, v2
	v_accvgpr_read_b32 v2, a47
	v_add_f32_e32 v2, v5, v2
	v_max_f32_e32 v20, 0, v2
	v_cvt_pk_f16_f32 v4, v9, v10
	v_cvt_pk_f16_f32 v3, v7, v8
	v_cvt_pk_f16_f32 v2, v1, v6
	ds_read_b128 v[6:9], v0 offset:47104
	v_cvt_pk_f16_f32 v5, v11, v12
	v_accvgpr_read_b32 v1, a16
	s_waitcnt lgkmcnt(0)
	v_mfma_f32_32x32x16_f16 a[32:47], v[6:9], v[2:5], 0
	ds_read_b128 v[6:9], v0 offset:48128
	v_cvt_pk_f16_f32 v5, v19, v20
	v_cvt_pk_f16_f32 v4, v17, v18
	v_cvt_pk_f16_f32 v3, v15, v16
	v_cvt_pk_f16_f32 v2, v13, v14
	v_accvgpr_read_b32 v13, a24
	v_accvgpr_read_b32 v17, a28
	s_waitcnt lgkmcnt(0)
	v_mfma_f32_32x32x16_f16 a[32:47], v[6:9], v[2:5], a[32:47]
	ds_read_b128 v[2:5], v22 offset:53760
	v_accvgpr_read_b32 v9, a20
	s_waitcnt lgkmcnt(0)
	v_add_f32_e32 v1, v1, v2
	v_accvgpr_read_b32 v2, a17
	v_add_f32_e32 v2, v3, v2
	v_max_f32_e32 v6, 0, v2
	v_accvgpr_read_b32 v2, a18
	v_add_f32_e32 v2, v4, v2
	v_max_f32_e32 v7, 0, v2
	v_accvgpr_read_b32 v2, a19
	v_add_f32_e32 v2, v5, v2
	v_max_f32_e32 v8, 0, v2
	ds_read_b128 v[2:5], v22 offset:53792
	v_max_f32_e32 v1, 0, v1
	s_waitcnt lgkmcnt(0)
	v_add_f32_e32 v2, v9, v2
	v_max_f32_e32 v9, 0, v2
	v_accvgpr_read_b32 v2, a21
	v_add_f32_e32 v2, v3, v2
	v_max_f32_e32 v10, 0, v2
	v_accvgpr_read_b32 v2, a22
	v_add_f32_e32 v2, v4, v2
	v_max_f32_e32 v11, 0, v2
	v_accvgpr_read_b32 v2, a23
	v_add_f32_e32 v2, v5, v2
	v_max_f32_e32 v12, 0, v2
	ds_read_b128 v[2:5], v22 offset:53824
	s_waitcnt lgkmcnt(0)
	v_add_f32_e32 v2, v13, v2
	v_max_f32_e32 v13, 0, v2
	v_accvgpr_read_b32 v2, a25
	v_add_f32_e32 v2, v3, v2
	v_max_f32_e32 v14, 0, v2
	v_accvgpr_read_b32 v2, a26
	v_add_f32_e32 v2, v4, v2
	v_max_f32_e32 v15, 0, v2
	v_accvgpr_read_b32 v2, a27
	v_add_f32_e32 v2, v5, v2
	v_max_f32_e32 v16, 0, v2
	ds_read_b128 v[2:5], v22 offset:53856
	s_waitcnt lgkmcnt(0)
	v_add_f32_e32 v2, v17, v2
	v_max_f32_e32 v17, 0, v2
	v_accvgpr_read_b32 v2, a29
	v_add_f32_e32 v2, v3, v2
	v_max_f32_e32 v18, 0, v2
	v_accvgpr_read_b32 v2, a30
	v_add_f32_e32 v2, v4, v2
	v_max_f32_e32 v19, 0, v2
	v_accvgpr_read_b32 v2, a31
	v_add_f32_e32 v2, v5, v2
	v_max_f32_e32 v20, 0, v2
	v_cvt_pk_f16_f32 v4, v9, v10
	v_cvt_pk_f16_f32 v3, v7, v8
	v_cvt_pk_f16_f32 v2, v1, v6
	ds_read_b128 v[6:9], v0 offset:49152
	v_cvt_pk_f16_f32 v5, v11, v12
	v_accvgpr_read_b32 v1, a0
	s_waitcnt lgkmcnt(0)
	v_mfma_f32_32x32x16_f16 a[32:47], v[6:9], v[2:5], a[32:47]
	ds_read_b128 v[6:9], v0 offset:50176
	v_cvt_pk_f16_f32 v5, v19, v20
	v_cvt_pk_f16_f32 v4, v17, v18
	v_cvt_pk_f16_f32 v3, v15, v16
	v_cvt_pk_f16_f32 v2, v13, v14
	v_accvgpr_read_b32 v13, a8
	v_accvgpr_read_b32 v17, a12
	s_waitcnt lgkmcnt(0)
	v_mfma_f32_32x32x16_f16 a[32:47], v[6:9], v[2:5], a[32:47]
	ds_read_b128 v[2:5], v22 offset:53888
	v_accvgpr_read_b32 v9, a4
	s_waitcnt lgkmcnt(0)
	v_add_f32_e32 v1, v1, v2
	v_accvgpr_read_b32 v2, a1
	v_add_f32_e32 v2, v3, v2
	v_max_f32_e32 v6, 0, v2
	v_accvgpr_read_b32 v2, a2
	v_add_f32_e32 v2, v4, v2
	v_max_f32_e32 v7, 0, v2
	v_accvgpr_read_b32 v2, a3
	v_add_f32_e32 v2, v5, v2
	v_max_f32_e32 v8, 0, v2
	ds_read_b128 v[2:5], v22 offset:53920
	v_max_f32_e32 v1, 0, v1
	s_waitcnt lgkmcnt(0)
	v_add_f32_e32 v2, v9, v2
	v_max_f32_e32 v9, 0, v2
	v_accvgpr_read_b32 v2, a5
	v_add_f32_e32 v2, v3, v2
	v_max_f32_e32 v10, 0, v2
	v_accvgpr_read_b32 v2, a6
	v_add_f32_e32 v2, v4, v2
	v_max_f32_e32 v11, 0, v2
	v_accvgpr_read_b32 v2, a7
	v_add_f32_e32 v2, v5, v2
	v_max_f32_e32 v12, 0, v2
	ds_read_b128 v[2:5], v22 offset:53952
	s_waitcnt lgkmcnt(0)
	v_add_f32_e32 v2, v13, v2
	v_max_f32_e32 v13, 0, v2
	v_accvgpr_read_b32 v2, a9
	v_add_f32_e32 v2, v3, v2
	v_max_f32_e32 v14, 0, v2
	v_accvgpr_read_b32 v2, a10
	v_add_f32_e32 v2, v4, v2
	v_max_f32_e32 v15, 0, v2
	v_accvgpr_read_b32 v2, a11
	v_add_f32_e32 v2, v5, v2
	v_max_f32_e32 v16, 0, v2
	ds_read_b128 v[2:5], v22 offset:53984
	s_waitcnt lgkmcnt(0)
	v_add_f32_e32 v2, v17, v2
	v_max_f32_e32 v17, 0, v2
	v_accvgpr_read_b32 v2, a13
	v_add_f32_e32 v2, v3, v2
	v_max_f32_e32 v18, 0, v2
	v_accvgpr_read_b32 v2, a14
	v_add_f32_e32 v2, v4, v2
	v_max_f32_e32 v19, 0, v2
	v_accvgpr_read_b32 v2, a15
	v_add_f32_e32 v2, v5, v2
	v_max_f32_e32 v20, 0, v2
	v_cvt_pk_f16_f32 v4, v9, v10
	v_cvt_pk_f16_f32 v3, v7, v8
	v_cvt_pk_f16_f32 v2, v1, v6
	ds_read_b128 v[6:9], v0 offset:51200
	v_cvt_pk_f16_f32 v5, v11, v12
	s_waitcnt lgkmcnt(0)
	s_nop 0
	v_mfma_f32_32x32x16_f16 a[32:47], v[6:9], v[2:5], a[32:47]
	ds_read_b128 v[6:9], v0 offset:52224
	v_cvt_pk_f16_f32 v5, v19, v20
	v_cvt_pk_f16_f32 v4, v17, v18
	v_cvt_pk_f16_f32 v3, v15, v16
	v_cvt_pk_f16_f32 v2, v13, v14
	s_waitcnt lgkmcnt(0)
	s_nop 0
	v_mfma_f32_32x32x16_f16 a[32:47], v[6:9], v[2:5], a[32:47]
	s_and_saveexec_b64 s[2:3], s[0:1]
	s_cbranch_execz .LBB3_39
	v_accvgpr_read_b32 v0, a80
	v_accvgpr_read_b32 v6, a86
	v_accvgpr_read_b32 v7, a87
	v_accvgpr_read_b32 v8, a88
	v_accvgpr_read_b32 v9, a89
	v_accvgpr_read_b32 v10, a90
	v_accvgpr_read_b32 v11, a91
	v_accvgpr_read_b32 v12, a92
	v_accvgpr_read_b32 v13, a93
	v_accvgpr_read_b32 v14, a94
	v_accvgpr_read_b32 v15, a95
	v_accvgpr_read_b32 v6, a32
	v_accvgpr_read_b32 v14, a40
	v_accvgpr_read_b32 v15, a41
	v_accvgpr_read_b32 v16, a42
	v_accvgpr_read_b32 v17, a43
	v_accvgpr_read_b32 v18, a44
	v_accvgpr_read_b32 v19, a45
	v_accvgpr_read_b32 v20, a46
	v_accvgpr_read_b32 v21, a47
	ds_read_b128 v[14:17], v22 offset:54016
	ds_read_b128 v[18:21], v22 offset:54080
	v_accvgpr_read_b32 v12, a38
	v_accvgpr_read_b32 v13, a39
	v_lshlrev_b32_e32 v24, 2, v85
	v_accvgpr_read_b32 v1, a81
	v_accvgpr_read_b32 v7, a33
	v_mad_i64_i32 v[12:13], s[0:1], v80, 40, s[18:19]
	v_ashrrev_i32_e32 v25, 31, v24
	v_accvgpr_read_b32 v3, a83
	v_accvgpr_read_b32 v9, a35
	v_lshl_add_u64 v[22:23], v[24:25], 2, v[12:13]
	v_mov_b32_e32 v25, v1
	s_waitcnt lgkmcnt(1)
	v_mov_b32_e32 v27, v15
	v_mov_b32_e32 v1, v7
	s_waitcnt lgkmcnt(0)
	v_mov_b32_e32 v15, v19
	v_accvgpr_read_b32 v2, a82
	v_accvgpr_read_b32 v8, a34
	v_pk_add_f32 v[0:1], v[0:1], v[14:15]
	v_mov_b32_e32 v7, v3
	v_mov_b32_e32 v15, v17
	v_mov_b32_e32 v3, v9
	v_mov_b32_e32 v17, v21
	v_mov_b32_e32 v24, v6
	v_mov_b32_e32 v26, v18
	v_mov_b32_e32 v6, v8
	v_mov_b32_e32 v14, v20
	v_pk_add_f32 v[2:3], v[2:3], v[16:17]
	v_pk_add_f32 v[24:25], v[24:25], v[26:27]
	s_waitcnt vmcnt(0)
	v_pk_mul_f32 v[0:1], v[82:83], v[0:1]
	v_pk_add_f32 v[6:7], v[6:7], v[14:15]
	v_pk_mul_f32 v[2:3], v[82:83], v[2:3]
	v_accvgpr_read_b32 v4, a84
	v_accvgpr_read_b32 v5, a85
	v_accvgpr_read_b32 v10, a36
	v_accvgpr_read_b32 v11, a37
	v_pk_fma_f32 v[0:1], v[82:83], v[24:25], v[0:1] op_sel:[1,0,0] op_sel_hi:[0,1,1]
	v_pk_fma_f32 v[2:3], v[82:83], v[6:7], v[2:3] op_sel:[1,0,0] op_sel_hi:[0,1,1]
	v_cmp_eq_u32_e32 vcc, 0, v85
	global_store_dwordx4 v[22:23], v[0:3], off
	s_and_b64 exec, exec, vcc
	s_cbranch_execz .LBB3_39
	s_mov_b32 s0, 0xd000
	v_add_u32_e64 v0, s0, 0
	ds_read2_b64 v[0:3], v0 offset0:100 offset1:108
	v_mov_b32_e32 v9, v5
	v_mov_b32_e32 v5, v11
	v_mov_b32_e32 v8, v10
	v_pk_mov_b32 v[6:7], v[82:83], v[82:83] op_sel:[1,0]
	s_waitcnt lgkmcnt(0)
	v_mov_b32_e32 v15, v1
	v_mov_b32_e32 v1, v3
	v_mov_b32_e32 v14, v2
	v_pk_add_f32 v[0:1], v[4:5], v[0:1]
	v_pk_add_f32 v[8:9], v[8:9], v[14:15]
	v_pk_mul_f32 v[0:1], v[82:83], v[0:1]
	s_nop 0
	v_pk_fma_f32 v[0:1], v[6:7], v[8:9], v[0:1]
	global_store_dwordx2 v[12:13], v[0:1], off offset:32
